# baseline (speedup 1.0000x reference)
_Z16bilateral_kernelPKfS0_Pf:
	s_load_dwordx2 s[4:5], s[0:1], 0x0
	s_load_dwordx2 s[8:9], s[0:1], 0x10
	s_lshr_b32 s19, s2, 8
	s_and_b32 s0, s2, 7
	s_mulk_i32 s0, 0x60
	s_lshr_b32 s1, s2, 3
	s_add_i32 s1, s0, s1
	s_lshr_b32 s0, s1, 6
	s_lshl_b32 s11, s1, 6
	s_nop 0
	s_and_b32 s11, s11, 0x1c0
	s_lshl_b32 s1, s1, 3
	s_nop 0
	s_and_b32 s10, s1, 0x1c0
	s_mov_b32 s1, 0
	s_lshl_b64 s[2:3], s[0:1], 20
	s_mov_b32 s20, 0xc05dfbe6
	s_mov_b32 s21, 0xc05dfbe6
	s_mov_b32 s22, 0xc0a8390e
	s_mov_b32 s23, 0xc0a8390e
	s_mov_b32 s24, 0xc08211a7
	s_mov_b32 s25, 0xc08211a7
	s_mov_b32 s26, 0xc0bb4cc1
	s_mov_b32 s27, 0xc0bb4cc1
	s_mov_b32 s28, 0xc0f487dc
	s_mov_b32 s29, 0xc0f487dc
	s_mov_b32 s30, 0x3e0bd796
	s_mov_b32 s31, 0x3e0bd796
	s_mov_b32 s32, 0x3f45a90c
	s_mov_b32 s33, 0x3f45a90c
	s_mov_b32 s34, 0x3fa5c782
	s_mov_b32 s35, 0x3fa5c782
	v_and_b32_e32 v118, 15, v0
	v_lshrrev_b32_e32 v115, 2, v0
	v_lshl_or_b32 v113, v118, 2, s11
	v_and_or_b32 v117, v115, 60, s10
	v_min_u32_e32 v116, 0x1fa, v113
	v_sub_u32_e64 v115, v113, 2 clamp
	v_add_u32_e64 v116, 4, v116
	v_cmp_eq_u32_e64 s[16:17], 0, v118
	v_cmp_eq_u32_e32 vcc, 15, v118
	s_nop 1
	v_cndmask_b32_e64 v115, v116, v115, s[16:17]
	s_or_b64 vcc, s[16:17], vcc
	v_lshlrev_b32_e32 v115, 2, v115
	v_mov_b32_e32 v116, 0x7ff00000
	s_nop 0
	v_cndmask_b32_e32 v112, v116, v115, vcc
	s_movk_i32 s18, 0x1fc
	v_cmp_eq_u32_e32 vcc, 0, v113
	v_cmp_eq_u32_e64 s[16:17], s18, v113
	v_lshlrev_b32_e32 v113, 2, v113
	s_waitcnt lgkmcnt(0)
	s_add_u32 s4, s4, s2
	s_addc_u32 s5, s5, s3
	s_and_b32 s5, s5, 0xffff
	s_mov_b32 s6, 0x100000
	s_mov_b32 s7, 0x20000
	s_add_u32 s12, s8, s2
	s_addc_u32 s13, s9, s3
	s_and_b32 s13, s13, 0xffff
	s_mov_b32 s14, 0x100000
	s_mov_b32 s15, 0x20000
	v_sub_u32_e64 v115, v117, 2 clamp
	v_lshlrev_b32_e32 v115, 11, v115
	v_add_u32_e32 v116, v115, v112
	v_add_u32_e64 v115, v115, v113
	buffer_load_dwordx2 v[0:1], v116, s[4:7], 0 offen nt
	buffer_load_dwordx2 v[6:7], v116, s[4:7], 0 offen nt
	buffer_load_dwordx4 v[2:5], v115, s[4:7], 0 offen nt
	v_sub_u32_e64 v115, v117, 1 clamp
	v_lshlrev_b32_e32 v115, 11, v115
	v_add_u32_e32 v116, v115, v112
	v_add_u32_e64 v115, v115, v113
	buffer_load_dwordx2 v[8:9], v116, s[4:7], 0 offen nt
	buffer_load_dwordx2 v[14:15], v116, s[4:7], 0 offen nt
	buffer_load_dwordx4 v[10:13], v115, s[4:7], 0 offen nt
	v_lshlrev_b32_e32 v115, 11, v117
	v_add_u32_e32 v116, v115, v112
	v_add_u32_e64 v114, v115, v113
	v_add_u32_e32 v119, 0x1000, v114
	buffer_load_dwordx2 v[16:17], v116, s[4:7], 0 offen nt
	buffer_load_dwordx2 v[22:23], v116, s[4:7], 0 offen nt
	buffer_load_dwordx4 v[18:21], v114, s[4:7], 0 offen nt
	v_lshlrev_b32_e64 v115, 11, v117
	v_add_u32_e32 v115, 0x800, v115
	v_add_u32_e32 v116, v115, v112
	v_add_u32_e32 v115, v115, v113
	buffer_load_dwordx2 v[24:25], v116, s[4:7], 0 offen nt
	buffer_load_dwordx2 v[30:31], v116, s[4:7], 0 offen nt
	buffer_load_dwordx4 v[26:29], v115, s[4:7], 0 offen nt
	v_lshlrev_b32_e64 v115, 11, v117
	v_add_u32_e32 v115, 0x1000, v115
	v_add_u32_e32 v116, v115, v112
	v_add_u32_e32 v115, v115, v113
	buffer_load_dwordx2 v[32:33], v116, s[4:7], 0 offen nt
	buffer_load_dwordx2 v[38:39], v116, s[4:7], 0 offen nt
	buffer_load_dwordx4 v[34:37], v115, s[4:7], 0 offen nt
	v_lshlrev_b32_e64 v115, 11, v117
	v_add_u32_e32 v115, 0x1800, v115
	v_add_u32_e32 v116, v115, v112
	v_add_u32_e32 v115, v115, v113
	buffer_load_dwordx2 v[40:41], v116, s[4:7], 0 offen nt
	buffer_load_dwordx2 v[46:47], v116, s[4:7], 0 offen nt
	buffer_load_dwordx4 v[42:45], v115, s[4:7], 0 offen nt
	v_min_u32_e32 v115, 0x1fb, v117
	v_lshlrev_b32_e64 v115, 11, v115
	v_add_u32_e32 v115, 0x2000, v115
	v_add_u32_e32 v116, v115, v112
	v_add_u32_e32 v115, v115, v113
	buffer_load_dwordx2 v[48:49], v116, s[4:7], 0 offen nt
	buffer_load_dwordx2 v[54:55], v116, s[4:7], 0 offen nt
	buffer_load_dwordx4 v[50:53], v115, s[4:7], 0 offen nt
	v_min_u32_e32 v115, 0x1fa, v117
	v_lshlrev_b32_e64 v115, 11, v115
	v_add_u32_e32 v115, 0x2800, v115
	v_add_u32_e32 v116, v115, v112
	v_add_u32_e32 v115, v115, v113
	buffer_load_dwordx2 v[56:57], v116, s[4:7], 0 offen nt
	buffer_load_dwordx2 v[62:63], v116, s[4:7], 0 offen nt
	buffer_load_dwordx4 v[58:61], v115, s[4:7], 0 offen nt
	s_waitcnt vmcnt(21)
	s_nop 0
	v_mov_b32_dpp v0, v4 row_shr:1 row_mask:0xf bank_mask:0xf
	v_mov_b32_dpp v1, v5 row_shr:1 row_mask:0xf bank_mask:0xf
	v_mov_b32_dpp v6, v2 row_shl:1 row_mask:0xf bank_mask:0xf
	v_mov_b32_dpp v7, v3 row_shl:1 row_mask:0xf bank_mask:0xf
	v_pk_mul_f32 v[2:3], v[2:3], s[32:33]
	v_pk_mul_f32 v[4:5], v[4:5], s[32:33]
	v_cndmask_b32_e64 v1, v1, v0, vcc
	v_cndmask_b32_e64 v6, v6, v7, s[16:17]
	v_pk_mul_f32 v[0:1], v[0:1], s[32:33]
	v_pk_mul_f32 v[6:7], v[6:7], s[32:33]
	s_waitcnt vmcnt(18)
	s_nop 0
	v_mov_b32_dpp v8, v12 row_shr:1 row_mask:0xf bank_mask:0xf
	v_mov_b32_dpp v9, v13 row_shr:1 row_mask:0xf bank_mask:0xf
	v_mov_b32_dpp v14, v10 row_shl:1 row_mask:0xf bank_mask:0xf
	v_mov_b32_dpp v15, v11 row_shl:1 row_mask:0xf bank_mask:0xf
	v_pk_mul_f32 v[10:11], v[10:11], s[32:33]
	v_pk_mul_f32 v[12:13], v[12:13], s[32:33]
	v_cndmask_b32_e64 v9, v9, v8, vcc
	v_cndmask_b32_e64 v14, v14, v15, s[16:17]
	v_pk_mul_f32 v[8:9], v[8:9], s[32:33]
	v_pk_mul_f32 v[14:15], v[14:15], s[32:33]
	s_waitcnt vmcnt(15)
	s_nop 0
	v_mov_b32_dpp v16, v20 row_shr:1 row_mask:0xf bank_mask:0xf
	v_mov_b32_dpp v17, v21 row_shr:1 row_mask:0xf bank_mask:0xf
	v_mov_b32_dpp v22, v18 row_shl:1 row_mask:0xf bank_mask:0xf
	v_mov_b32_dpp v23, v19 row_shl:1 row_mask:0xf bank_mask:0xf
	v_pk_mul_f32 v[18:19], v[18:19], s[32:33]
	v_pk_mul_f32 v[20:21], v[20:21], s[32:33]
	v_cndmask_b32_e64 v17, v17, v16, vcc
	v_cndmask_b32_e64 v22, v22, v23, s[16:17]
	v_pk_mul_f32 v[68:69], v[18:19], s[30:31]
	v_pk_mul_f32 v[70:71], v[20:21], s[30:31]
	v_pk_mul_f32 v[16:17], v[16:17], s[32:33]
	v_pk_mul_f32 v[22:23], v[22:23], s[32:33]
	s_cmp_eq_u32 s19, 0
	s_cbranch_scc1 .Lmyha2
	s_setprio 3
	s_branch .Lmyhb2
.Lmyha2:
	s_setprio 3
.Lmyhb2:
	s_nop 0
	v_pk_add_f32 v[96:97], v[18:19], v[0:1] neg_lo:[0,1] neg_hi:[0,1]
	v_pk_add_f32 v[98:99], v[18:19], v[2:3] neg_lo:[0,1] neg_hi:[0,1]
	v_pk_add_f32 v[100:101], v[20:21], v[2:3] neg_lo:[0,1] neg_hi:[0,1]
	v_pk_add_f32 v[102:103], v[18:19], v[4:5] neg_lo:[0,1] neg_hi:[0,1]
	v_pk_fma_f32 v[96:97], v[96:97], v[96:97], s[28:29] neg_lo:[1,0,0] neg_hi:[1,0,0]
	v_pk_fma_f32 v[98:99], v[98:99], v[98:99], s[22:23] neg_lo:[1,0,0] neg_hi:[1,0,0]
	v_pk_fma_f32 v[100:101], v[100:101], v[100:101], s[28:29] neg_lo:[1,0,0] neg_hi:[1,0,0]
	v_pk_fma_f32 v[102:103], v[102:103], v[102:103], s[28:29] neg_lo:[1,0,0] neg_hi:[1,0,0]
	v_exp_f32_e32 v96, v96
	v_exp_f32_e32 v97, v97
	v_exp_f32_e32 v98, v98
	v_exp_f32_e32 v99, v99
	v_exp_f32_e32 v100, v100
	v_exp_f32_e32 v101, v101
	v_exp_f32_e32 v102, v102
	v_exp_f32_e32 v103, v103
	v_pk_add_f32 v[104:105], v[20:21], v[4:5] neg_lo:[0,1] neg_hi:[0,1]
	v_pk_add_f32 v[106:107], v[20:21], v[6:7] neg_lo:[0,1] neg_hi:[0,1]
	v_pk_add_f32 v[108:109], v[18:19], v[2:3] op_sel:[1,0] op_sel_hi:[0,1] neg_lo:[0,1] neg_hi:[0,1]
	v_pk_add_f32 v[110:111], v[20:21], v[4:5] op_sel:[1,0] op_sel_hi:[0,1] neg_lo:[0,1] neg_hi:[0,1]
	v_pk_fma_f32 v[104:105], v[104:105], v[104:105], s[22:23] neg_lo:[1,0,0] neg_hi:[1,0,0]
	v_pk_fma_f32 v[106:107], v[106:107], v[106:107], s[28:29] neg_lo:[1,0,0] neg_hi:[1,0,0]
	v_pk_fma_f32 v[108:109], v[108:109], v[108:109], s[26:27] neg_lo:[1,0,0] neg_hi:[1,0,0]
	v_pk_fma_f32 v[110:111], v[110:111], v[110:111], s[26:27] neg_lo:[1,0,0] neg_hi:[1,0,0]
	v_exp_f32_e32 v104, v104
	v_exp_f32_e32 v105, v105
	v_exp_f32_e32 v106, v106
	v_exp_f32_e32 v107, v107
	v_exp_f32_e32 v108, v108
	v_exp_f32_e32 v109, v109
	v_exp_f32_e32 v110, v110
	v_exp_f32_e32 v111, v111
	v_pk_add_f32 v[64:65], s[30:31], v[96:97]
	v_pk_fma_f32 v[68:69], v[96:97], v[0:1], v[68:69]
	v_pk_add_f32 v[66:67], s[30:31], v[100:101]
	v_pk_add_f32 v[64:65], v[64:65], v[98:99]
	v_pk_fma_f32 v[68:69], v[98:99], v[2:3], v[68:69]
	v_pk_fma_f32 v[70:71], v[100:101], v[2:3], v[70:71]
	v_pk_add_f32 v[64:65], v[64:65], v[102:103]
	v_pk_fma_f32 v[68:69], v[102:103], v[4:5], v[68:69]
	v_pk_add_f32 v[96:97], v[18:19], v[8:9] neg_lo:[0,1] neg_hi:[0,1]
	v_pk_add_f32 v[98:99], v[18:19], v[10:11] neg_lo:[0,1] neg_hi:[0,1]
	v_pk_add_f32 v[100:101], v[20:21], v[10:11] neg_lo:[0,1] neg_hi:[0,1]
	v_pk_add_f32 v[102:103], v[18:19], v[12:13] neg_lo:[0,1] neg_hi:[0,1]
	v_pk_fma_f32 v[96:97], v[96:97], v[96:97], s[26:27] neg_lo:[1,0,0] neg_hi:[1,0,0]
	v_pk_fma_f32 v[98:99], v[98:99], v[98:99], s[20:21] neg_lo:[1,0,0] neg_hi:[1,0,0]
	v_pk_fma_f32 v[100:101], v[100:101], v[100:101], s[26:27] neg_lo:[1,0,0] neg_hi:[1,0,0]
	v_pk_fma_f32 v[102:103], v[102:103], v[102:103], s[26:27] neg_lo:[1,0,0] neg_hi:[1,0,0]
	v_exp_f32_e32 v96, v96
	v_exp_f32_e32 v97, v97
	v_exp_f32_e32 v98, v98
	v_exp_f32_e32 v99, v99
	v_exp_f32_e32 v100, v100
	v_exp_f32_e32 v101, v101
	v_exp_f32_e32 v102, v102
	v_exp_f32_e32 v103, v103
	v_pk_add_f32 v[66:67], v[66:67], v[104:105]
	v_pk_fma_f32 v[70:71], v[104:105], v[4:5], v[70:71]
	v_pk_add_f32 v[64:65], v[64:65], v[108:109] op_sel:[0,1] op_sel_hi:[1,0]
	v_pk_add_f32 v[66:67], v[66:67], v[106:107]
	v_pk_fma_f32 v[70:71], v[106:107], v[6:7], v[70:71]
	v_pk_fma_f32 v[68:69], v[108:109], v[2:3], v[68:69] op_sel:[1,1,0] op_sel_hi:[0,0,1]
	v_pk_add_f32 v[66:67], v[66:67], v[110:111] op_sel:[0,1] op_sel_hi:[1,0]
	v_pk_fma_f32 v[70:71], v[110:111], v[4:5], v[70:71] op_sel:[1,1,0] op_sel_hi:[0,0,1]
	v_pk_add_f32 v[104:105], v[20:21], v[12:13] neg_lo:[0,1] neg_hi:[0,1]
	v_pk_add_f32 v[106:107], v[20:21], v[14:15] neg_lo:[0,1] neg_hi:[0,1]
	v_pk_add_f32 v[108:109], v[18:19], v[10:11] op_sel:[1,0] op_sel_hi:[0,1] neg_lo:[0,1] neg_hi:[0,1]
	v_pk_add_f32 v[110:111], v[20:21], v[12:13] op_sel:[1,0] op_sel_hi:[0,1] neg_lo:[0,1] neg_hi:[0,1]
	v_pk_fma_f32 v[104:105], v[104:105], v[104:105], s[20:21] neg_lo:[1,0,0] neg_hi:[1,0,0]
	v_pk_fma_f32 v[106:107], v[106:107], v[106:107], s[26:27] neg_lo:[1,0,0] neg_hi:[1,0,0]
	v_pk_fma_f32 v[108:109], v[108:109], v[108:109], s[24:25] neg_lo:[1,0,0] neg_hi:[1,0,0]
	v_pk_fma_f32 v[110:111], v[110:111], v[110:111], s[24:25] neg_lo:[1,0,0] neg_hi:[1,0,0]
	v_exp_f32_e32 v104, v104
	v_exp_f32_e32 v105, v105
	v_exp_f32_e32 v106, v106
	v_exp_f32_e32 v107, v107
	v_exp_f32_e32 v108, v108
	v_exp_f32_e32 v109, v109
	v_exp_f32_e32 v110, v110
	v_exp_f32_e32 v111, v111
	v_pk_add_f32 v[64:65], v[64:65], v[96:97]
	v_pk_fma_f32 v[68:69], v[96:97], v[8:9], v[68:69]
	v_pk_add_f32 v[66:67], v[66:67], v[100:101]
	v_pk_add_f32 v[64:65], v[64:65], v[98:99]
	v_pk_fma_f32 v[68:69], v[98:99], v[10:11], v[68:69]
	v_pk_fma_f32 v[70:71], v[100:101], v[10:11], v[70:71]
	v_pk_add_f32 v[64:65], v[64:65], v[102:103]
	v_pk_fma_f32 v[68:69], v[102:103], v[12:13], v[68:69]
	v_pk_add_f32 v[96:97], v[18:19], v[16:17] neg_lo:[0,1] neg_hi:[0,1]
	v_pk_add_f32 v[98:99], v[20:21], v[18:19] neg_lo:[0,1] neg_hi:[0,1]
	v_pk_add_f32 v[100:101], v[22:23], v[20:21] neg_lo:[0,1] neg_hi:[0,1]
	v_pk_fma_f32 v[96:97], v[96:97], v[96:97], s[22:23] neg_lo:[1,0,0] neg_hi:[1,0,0]
	v_pk_fma_f32 v[98:99], v[98:99], v[98:99], s[22:23] neg_lo:[1,0,0] neg_hi:[1,0,0]
	v_pk_fma_f32 v[100:101], v[100:101], v[100:101], s[22:23] neg_lo:[1,0,0] neg_hi:[1,0,0]
	v_exp_f32_e32 v96, v96
	v_exp_f32_e32 v97, v97
	v_exp_f32_e32 v98, v98
	v_exp_f32_e32 v99, v99
	v_exp_f32_e32 v100, v100
	v_exp_f32_e32 v101, v101
	v_pk_add_f32 v[66:67], v[66:67], v[104:105]
	v_pk_fma_f32 v[70:71], v[104:105], v[12:13], v[70:71]
	v_pk_add_f32 v[64:65], v[64:65], v[108:109] op_sel:[0,1] op_sel_hi:[1,0]
	v_pk_add_f32 v[66:67], v[66:67], v[106:107]
	v_pk_fma_f32 v[70:71], v[106:107], v[14:15], v[70:71]
	v_pk_fma_f32 v[68:69], v[108:109], v[10:11], v[68:69] op_sel:[1,1,0] op_sel_hi:[0,0,1]
	v_pk_add_f32 v[66:67], v[66:67], v[110:111] op_sel:[0,1] op_sel_hi:[1,0]
	v_pk_fma_f32 v[70:71], v[110:111], v[12:13], v[70:71] op_sel:[1,1,0] op_sel_hi:[0,0,1]
	v_sub_f32_e32 v104, v18, v1
	v_sub_f32_e32 v106, v20, v3
	v_sub_f32_e32 v108, v19, v4
	v_sub_f32_e32 v110, v21, v6
	v_sub_f32_e32 v105, v18, v9
	v_sub_f32_e32 v107, v20, v11
	v_sub_f32_e32 v109, v19, v12
	v_sub_f32_e32 v111, v21, v14
	v_fma_f32 v104, -v104, v104, s26
	v_fma_f32 v106, -v106, v106, s26
	v_fma_f32 v108, -v108, v108, s26
	v_fma_f32 v110, -v110, v110, s26
	v_fma_f32 v105, -v105, v105, s24
	v_fma_f32 v107, -v107, v107, s24
	v_fma_f32 v109, -v109, v109, s24
	v_fma_f32 v111, -v111, v111, s24
	v_exp_f32_e32 v104, v104
	v_exp_f32_e32 v106, v106
	v_exp_f32_e32 v108, v108
	v_exp_f32_e32 v110, v110
	v_exp_f32_e32 v105, v105
	v_exp_f32_e32 v107, v107
	v_exp_f32_e32 v109, v109
	v_exp_f32_e32 v111, v111
	v_pk_add_f32 v[64:65], v[64:65], v[96:97]
	v_pk_fma_f32 v[68:69], v[96:97], v[16:17], v[68:69]
	v_pk_add_f32 v[66:67], v[66:67], v[98:99]
	v_pk_add_f32 v[64:65], v[64:65], v[98:99]
	v_pk_fma_f32 v[68:69], v[98:99], v[20:21], v[68:69]
	v_pk_fma_f32 v[70:71], v[98:99], v[18:19], v[70:71]
	v_pk_add_f32 v[66:67], v[66:67], v[100:101]
	v_pk_fma_f32 v[70:71], v[100:101], v[22:23], v[70:71]
	v_sub_f32_e32 v100, v18, v17
	v_sub_f32_e32 v96, v19, v18
	v_sub_f32_e32 v102, v20, v19
	v_sub_f32_e32 v98, v21, v20
	v_sub_f32_e64 v97, v22, v21
	v_fma_f32 v100, -v100, v100, s20
	v_fma_f32 v96, -v96, v96, s20
	v_fma_f32 v102, -v102, v102, s20
	v_fma_f32 v98, -v98, v98, s20
	v_fma_f32 v97, -v97, v97, s20
	v_exp_f32_e32 v100, v100
	v_exp_f32_e32 v96, v96
	v_exp_f32_e32 v102, v102
	v_exp_f32_e32 v98, v98
	v_exp_f32_e32 v97, v97
	v_add_f32_e32 v64, v64, v104
	v_fmac_f32_e32 v68, v104, v1
	v_add_f32_e32 v66, v66, v106
	v_fmac_f32_e32 v70, v106, v3
	v_add_f32_e32 v65, v65, v108
	v_fmac_f32_e32 v69, v108, v4
	v_add_f32_e32 v67, v67, v110
	v_fmac_f32_e32 v71, v110, v6
	v_add_f32_e32 v64, v64, v105
	v_fmac_f32_e32 v68, v105, v9
	v_add_f32_e32 v66, v66, v107
	v_fmac_f32_e32 v70, v107, v11
	v_add_f32_e32 v65, v65, v109
	v_fmac_f32_e32 v69, v109, v12
	v_add_f32_e32 v67, v67, v111
	v_fmac_f32_e32 v71, v111, v14
	v_add_f32_e32 v64, v64, v100
	v_fmac_f32_e32 v68, v100, v17
	v_add_f32_e32 v65, v65, v102
	v_fmac_f32_e32 v69, v102, v20
	v_add_f32_e32 v66, v66, v102
	v_fmac_f32_e32 v70, v102, v19
	v_add_f32_e32 v67, v67, v97
	v_fmac_f32_e64 v71, v97, v22
	v_pk_add_f32 v[64:65], v[64:65], v[96:97] op_sel_hi:[1,0]
	v_pk_fma_f32 v[68:69], v[96:97], v[18:19], v[68:69] op_sel:[0,1,0] op_sel_hi:[0,0,1]
	v_pk_add_f32 v[66:67], v[66:67], v[98:99] op_sel_hi:[1,0]
	v_pk_fma_f32 v[70:71], v[98:99], v[20:21], v[70:71] op_sel:[0,1,0] op_sel_hi:[0,0,1]
	s_waitcnt vmcnt(12)
	s_nop 0
	v_mov_b32_dpp v24, v28 row_shr:1 row_mask:0xf bank_mask:0xf
	v_mov_b32_dpp v25, v29 row_shr:1 row_mask:0xf bank_mask:0xf
	v_mov_b32_dpp v30, v26 row_shl:1 row_mask:0xf bank_mask:0xf
	v_mov_b32_dpp v31, v27 row_shl:1 row_mask:0xf bank_mask:0xf
	v_pk_mul_f32 v[26:27], v[26:27], s[32:33]
	v_pk_mul_f32 v[28:29], v[28:29], s[32:33]
	v_cndmask_b32_e64 v25, v25, v24, vcc
	v_cndmask_b32_e64 v30, v30, v31, s[16:17]
	v_pk_mul_f32 v[76:77], v[26:27], s[30:31]
	v_pk_mul_f32 v[78:79], v[28:29], s[30:31]
	v_pk_mul_f32 v[24:25], v[24:25], s[32:33]
	v_pk_mul_f32 v[30:31], v[30:31], s[32:33]
	s_cmp_eq_u32 s19, 0
	s_cbranch_scc1 .Lmyha3
	s_setprio 3
	s_branch .Lmyhb3

.Lmyhb3:
	s_nop 0
	v_pk_add_f32 v[96:97], v[26:27], v[8:9] neg_lo:[0,1] neg_hi:[0,1]
	v_pk_add_f32 v[98:99], v[26:27], v[10:11] neg_lo:[0,1] neg_hi:[0,1]
	v_pk_add_f32 v[100:101], v[28:29], v[10:11] neg_lo:[0,1] neg_hi:[0,1]
	v_pk_add_f32 v[102:103], v[26:27], v[12:13] neg_lo:[0,1] neg_hi:[0,1]
	v_pk_fma_f32 v[96:97], v[96:97], v[96:97], s[28:29] neg_lo:[1,0,0] neg_hi:[1,0,0]
	v_pk_fma_f32 v[98:99], v[98:99], v[98:99], s[22:23] neg_lo:[1,0,0] neg_hi:[1,0,0]
	v_pk_fma_f32 v[100:101], v[100:101], v[100:101], s[28:29] neg_lo:[1,0,0] neg_hi:[1,0,0]
	v_pk_fma_f32 v[102:103], v[102:103], v[102:103], s[28:29] neg_lo:[1,0,0] neg_hi:[1,0,0]
	v_exp_f32_e32 v96, v96
	v_exp_f32_e32 v97, v97
	v_exp_f32_e32 v98, v98
	v_exp_f32_e32 v99, v99
	v_exp_f32_e32 v100, v100
	v_exp_f32_e32 v101, v101
	v_exp_f32_e32 v102, v102
	v_exp_f32_e32 v103, v103
	v_pk_add_f32 v[104:105], v[28:29], v[12:13] neg_lo:[0,1] neg_hi:[0,1]
	v_pk_add_f32 v[106:107], v[28:29], v[14:15] neg_lo:[0,1] neg_hi:[0,1]
	v_pk_add_f32 v[108:109], v[26:27], v[10:11] op_sel:[1,0] op_sel_hi:[0,1] neg_lo:[0,1] neg_hi:[0,1]
	v_pk_add_f32 v[110:111], v[28:29], v[12:13] op_sel:[1,0] op_sel_hi:[0,1] neg_lo:[0,1] neg_hi:[0,1]
	v_pk_fma_f32 v[104:105], v[104:105], v[104:105], s[22:23] neg_lo:[1,0,0] neg_hi:[1,0,0]
	v_pk_fma_f32 v[106:107], v[106:107], v[106:107], s[28:29] neg_lo:[1,0,0] neg_hi:[1,0,0]
	v_pk_fma_f32 v[108:109], v[108:109], v[108:109], s[26:27] neg_lo:[1,0,0] neg_hi:[1,0,0]
	v_pk_fma_f32 v[110:111], v[110:111], v[110:111], s[26:27] neg_lo:[1,0,0] neg_hi:[1,0,0]
	v_exp_f32_e32 v104, v104
	v_exp_f32_e32 v105, v105
	v_exp_f32_e32 v106, v106
	v_exp_f32_e32 v107, v107
	v_exp_f32_e32 v108, v108
	v_exp_f32_e32 v109, v109
	v_exp_f32_e32 v110, v110
	v_exp_f32_e32 v111, v111
	v_pk_add_f32 v[72:73], s[30:31], v[96:97]
	v_pk_fma_f32 v[76:77], v[96:97], v[8:9], v[76:77]
	v_pk_add_f32 v[74:75], s[30:31], v[100:101]
	v_pk_add_f32 v[72:73], v[72:73], v[98:99]
	v_pk_fma_f32 v[76:77], v[98:99], v[10:11], v[76:77]
	v_pk_fma_f32 v[78:79], v[100:101], v[10:11], v[78:79]
	v_pk_add_f32 v[72:73], v[72:73], v[102:103]
	v_pk_fma_f32 v[76:77], v[102:103], v[12:13], v[76:77]
	v_pk_add_f32 v[96:97], v[26:27], v[16:17] neg_lo:[0,1] neg_hi:[0,1]
	v_pk_add_f32 v[98:99], v[24:25], v[18:19] neg_lo:[0,1] neg_hi:[0,1]
	v_pk_add_f32 v[100:101], v[26:27], v[18:19] neg_lo:[0,1] neg_hi:[0,1]
	v_pk_add_f32 v[102:103], v[28:29], v[18:19] neg_lo:[0,1] neg_hi:[0,1]
	v_pk_fma_f32 v[96:97], v[96:97], v[96:97], s[26:27] neg_lo:[1,0,0] neg_hi:[1,0,0]
	v_pk_fma_f32 v[98:99], v[98:99], v[98:99], s[26:27] neg_lo:[1,0,0] neg_hi:[1,0,0]
	v_pk_fma_f32 v[100:101], v[100:101], v[100:101], s[20:21] neg_lo:[1,0,0] neg_hi:[1,0,0]
	v_pk_fma_f32 v[102:103], v[102:103], v[102:103], s[26:27] neg_lo:[1,0,0] neg_hi:[1,0,0]
	v_exp_f32_e32 v96, v96
	v_exp_f32_e32 v97, v97
	v_exp_f32_e32 v98, v98
	v_exp_f32_e32 v99, v99
	v_exp_f32_e32 v100, v100
	v_exp_f32_e32 v101, v101
	v_exp_f32_e32 v102, v102
	v_exp_f32_e32 v103, v103
	v_pk_add_f32 v[74:75], v[74:75], v[104:105]
	v_pk_fma_f32 v[78:79], v[104:105], v[12:13], v[78:79]
	v_pk_add_f32 v[72:73], v[72:73], v[108:109] op_sel:[0,1] op_sel_hi:[1,0]
	v_pk_add_f32 v[74:75], v[74:75], v[106:107]
	v_pk_fma_f32 v[78:79], v[106:107], v[14:15], v[78:79]
	v_pk_fma_f32 v[76:77], v[108:109], v[10:11], v[76:77] op_sel:[1,1,0] op_sel_hi:[0,0,1]
	v_pk_add_f32 v[74:75], v[74:75], v[110:111] op_sel:[0,1] op_sel_hi:[1,0]
	v_pk_fma_f32 v[78:79], v[110:111], v[12:13], v[78:79] op_sel:[1,1,0] op_sel_hi:[0,0,1]
	v_pk_add_f32 v[104:105], v[26:27], v[20:21] neg_lo:[0,1] neg_hi:[0,1]
	v_pk_add_f32 v[106:107], v[28:29], v[20:21] neg_lo:[0,1] neg_hi:[0,1]
	v_pk_add_f32 v[108:109], v[30:31], v[20:21] neg_lo:[0,1] neg_hi:[0,1]
	v_pk_add_f32 v[110:111], v[28:29], v[22:23] neg_lo:[0,1] neg_hi:[0,1]
	v_pk_fma_f32 v[104:105], v[104:105], v[104:105], s[26:27] neg_lo:[1,0,0] neg_hi:[1,0,0]
	v_pk_fma_f32 v[106:107], v[106:107], v[106:107], s[20:21] neg_lo:[1,0,0] neg_hi:[1,0,0]
	v_pk_fma_f32 v[108:109], v[108:109], v[108:109], s[26:27] neg_lo:[1,0,0] neg_hi:[1,0,0]
	v_pk_fma_f32 v[110:111], v[110:111], v[110:111], s[26:27] neg_lo:[1,0,0] neg_hi:[1,0,0]
	v_exp_f32_e32 v104, v104
	v_exp_f32_e32 v105, v105
	v_exp_f32_e32 v106, v106
	v_exp_f32_e32 v107, v107
	v_exp_f32_e32 v108, v108
	v_exp_f32_e32 v109, v109
	v_exp_f32_e32 v110, v110
	v_exp_f32_e32 v111, v111
	v_pk_add_f32 v[72:73], v[72:73], v[96:97]
	v_pk_fma_f32 v[76:77], v[96:97], v[16:17], v[76:77]
	v_pk_add_f32 v[64:65], v[64:65], v[98:99]
	v_pk_fma_f32 v[68:69], v[98:99], v[24:25], v[68:69]
	v_pk_add_f32 v[72:73], v[72:73], v[100:101]
	v_pk_add_f32 v[64:65], v[64:65], v[100:101]
	v_pk_fma_f32 v[68:69], v[100:101], v[26:27], v[68:69]
	v_pk_fma_f32 v[76:77], v[100:101], v[18:19], v[76:77]
	v_pk_add_f32 v[64:65], v[64:65], v[102:103]
	v_pk_fma_f32 v[68:69], v[102:103], v[28:29], v[68:69]
	v_pk_add_f32 v[74:75], v[74:75], v[102:103]
	v_pk_fma_f32 v[78:79], v[102:103], v[18:19], v[78:79]
	v_pk_add_f32 v[96:97], v[26:27], v[18:19] op_sel:[1,0] op_sel_hi:[0,1] neg_lo:[0,1] neg_hi:[0,1]
	v_pk_add_f32 v[98:99], v[28:29], v[20:21] op_sel:[1,0] op_sel_hi:[0,1] neg_lo:[0,1] neg_hi:[0,1]
	v_pk_add_f32 v[100:101], v[26:27], v[24:25] neg_lo:[0,1] neg_hi:[0,1]
	v_pk_add_f32 v[102:103], v[28:29], v[26:27] neg_lo:[0,1] neg_hi:[0,1]
	v_pk_fma_f32 v[96:97], v[96:97], v[96:97], s[24:25] neg_lo:[1,0,0] neg_hi:[1,0,0]
	v_pk_fma_f32 v[98:99], v[98:99], v[98:99], s[24:25] neg_lo:[1,0,0] neg_hi:[1,0,0]
	v_pk_fma_f32 v[100:101], v[100:101], v[100:101], s[22:23] neg_lo:[1,0,0] neg_hi:[1,0,0]
	v_pk_fma_f32 v[102:103], v[102:103], v[102:103], s[22:23] neg_lo:[1,0,0] neg_hi:[1,0,0]
	v_exp_f32_e32 v96, v96
	v_exp_f32_e32 v97, v97
	v_exp_f32_e32 v98, v98
	v_exp_f32_e32 v99, v99
	v_exp_f32_e32 v100, v100
	v_exp_f32_e32 v101, v101
	v_exp_f32_e32 v102, v102
	v_exp_f32_e32 v103, v103
	v_pk_add_f32 v[66:67], v[66:67], v[104:105]
	v_pk_fma_f32 v[70:71], v[104:105], v[26:27], v[70:71]
	v_pk_add_f32 v[72:73], v[72:73], v[104:105]
	v_pk_fma_f32 v[76:77], v[104:105], v[20:21], v[76:77]
	v_pk_add_f32 v[66:67], v[66:67], v[106:107]
	v_pk_fma_f32 v[70:71], v[106:107], v[28:29], v[70:71]
	v_pk_add_f32 v[74:75], v[74:75], v[106:107]
	v_pk_fma_f32 v[78:79], v[106:107], v[20:21], v[78:79]
	v_pk_add_f32 v[66:67], v[66:67], v[108:109]
	v_pk_fma_f32 v[70:71], v[108:109], v[30:31], v[70:71]
	v_pk_add_f32 v[74:75], v[74:75], v[110:111]
	v_pk_fma_f32 v[78:79], v[110:111], v[22:23], v[78:79]
	v_pk_add_f32 v[104:105], v[30:31], v[28:29] neg_lo:[0,1] neg_hi:[0,1]
	v_pk_fma_f32 v[104:105], v[104:105], v[104:105], s[22:23] neg_lo:[1,0,0] neg_hi:[1,0,0]
	s_nop 0
	v_exp_f32_e32 v104, v104
	v_exp_f32_e64 v105, v105
	v_pk_add_f32 v[64:65], v[64:65], v[96:97]
	v_pk_fma_f32 v[68:69], v[96:97], v[26:27], v[68:69] op_sel:[0,1,0] op_sel_hi:[1,0,1]
	v_pk_add_f32 v[72:73], v[72:73], v[96:97] op_sel:[0,1] op_sel_hi:[1,0]
	v_pk_fma_f32 v[76:77], v[96:97], v[18:19], v[76:77] op_sel:[1,1,0] op_sel_hi:[0,0,1]
	v_pk_add_f32 v[66:67], v[66:67], v[98:99]
	v_pk_fma_f32 v[70:71], v[98:99], v[28:29], v[70:71] op_sel:[0,1,0] op_sel_hi:[1,0,1]
	v_pk_add_f32 v[74:75], v[74:75], v[98:99] op_sel:[0,1] op_sel_hi:[1,0]
	v_pk_fma_f32 v[78:79], v[98:99], v[20:21], v[78:79] op_sel:[1,1,0] op_sel_hi:[0,0,1]
	v_pk_add_f32 v[72:73], v[72:73], v[100:101]
	v_pk_fma_f32 v[76:77], v[100:101], v[24:25], v[76:77]
	v_pk_add_f32 v[74:75], v[74:75], v[102:103]
	v_pk_add_f32 v[72:73], v[72:73], v[102:103]
	v_pk_fma_f32 v[76:77], v[102:103], v[28:29], v[76:77]
	v_pk_fma_f32 v[78:79], v[102:103], v[26:27], v[78:79]
	s_nop 0
	v_sub_f32_e32 v96, v26, v9
	v_sub_f32_e32 v98, v28, v11
	v_sub_f32_e32 v100, v27, v12
	v_sub_f32_e32 v102, v29, v14
	v_sub_f32_e32 v97, v26, v17
	v_sub_f32_e32 v99, v25, v18
	v_sub_f32_e32 v101, v28, v19
	v_sub_f32_e64 v103, v27, v20
	v_fma_f32 v96, -v96, v96, s26
	v_fma_f32 v98, -v98, v98, s26
	v_fma_f32 v100, -v100, v100, s26
	v_fma_f32 v102, -v102, v102, s26
	v_fma_f32 v97, -v97, v97, s24
	v_fma_f32 v99, -v99, v99, s24
	v_fma_f32 v101, -v101, v101, s24
	v_fma_f32 v103, -v103, v103, s24
	v_exp_f32_e32 v96, v96
	v_exp_f32_e32 v98, v98
	v_exp_f32_e32 v100, v100
	v_exp_f32_e32 v102, v102
	v_exp_f32_e32 v97, v97
	v_exp_f32_e32 v99, v99
	v_exp_f32_e32 v101, v101
	v_exp_f32_e32 v103, v103
	v_pk_add_f32 v[74:75], v[74:75], v[104:105]
	v_pk_fma_f32 v[78:79], v[104:105], v[30:31], v[78:79]
	v_sub_f32_e32 v108, v30, v21
	v_sub_f32_e32 v110, v29, v22
	v_sub_f32_e32 v105, v26, v25
	v_sub_f32_e32 v104, v27, v26
	v_sub_f32_e32 v107, v28, v27
	v_sub_f32_e32 v106, v29, v28
	v_sub_f32_e64 v109, v30, v29
	v_fma_f32 v108, -v108, v108, s24
	v_fma_f32 v110, -v110, v110, s24
	v_fma_f32 v105, -v105, v105, s20
	v_fma_f32 v104, -v104, v104, s20
	v_fma_f32 v107, -v107, v107, s20
	v_fma_f32 v106, -v106, v106, s20
	v_fma_f32 v109, -v109, v109, s20
	v_exp_f32_e32 v108, v108
	v_exp_f32_e32 v110, v110
	v_exp_f32_e32 v105, v105
	v_exp_f32_e32 v104, v104
	v_exp_f32_e32 v107, v107
	v_exp_f32_e32 v106, v106
	v_exp_f32_e32 v109, v109
	v_add_f32_e32 v72, v72, v96
	v_fmac_f32_e32 v76, v96, v9
	v_add_f32_e32 v74, v74, v98
	v_fmac_f32_e32 v78, v98, v11
	v_add_f32_e32 v73, v73, v100
	v_fmac_f32_e32 v77, v100, v12
	v_add_f32_e32 v75, v75, v102
	v_fmac_f32_e32 v79, v102, v14
	v_add_f32_e32 v72, v72, v97
	v_fmac_f32_e32 v76, v97, v17
	v_add_f32_e32 v64, v64, v99
	v_fmac_f32_e32 v68, v99, v25
	v_add_f32_e32 v65, v65, v101
	v_fmac_f32_e32 v69, v101, v28
	v_add_f32_e32 v74, v74, v101
	v_fmac_f32_e32 v78, v101, v19
	v_add_f32_e32 v66, v66, v103
	v_fmac_f32_e32 v70, v103, v27
	v_add_f32_e32 v73, v73, v103
	v_fmac_f32_e32 v77, v103, v20
	v_add_f32_e32 v67, v67, v108
	v_fmac_f32_e32 v71, v108, v30
	v_add_f32_e32 v75, v75, v110
	v_fmac_f32_e32 v79, v110, v22
	v_add_f32_e32 v72, v72, v105
	v_fmac_f32_e32 v76, v105, v25
	v_add_f32_e32 v73, v73, v107
	v_fmac_f32_e32 v77, v107, v28
	v_add_f32_e32 v74, v74, v107
	v_fmac_f32_e32 v78, v107, v27
	v_add_f32_e32 v75, v75, v109
	v_fmac_f32_e64 v79, v109, v30
	v_pk_add_f32 v[72:73], v[72:73], v[104:105] op_sel_hi:[1,0]
	v_pk_fma_f32 v[76:77], v[104:105], v[26:27], v[76:77] op_sel:[0,1,0] op_sel_hi:[0,0,1]
	v_pk_add_f32 v[74:75], v[74:75], v[106:107] op_sel_hi:[1,0]
	v_pk_fma_f32 v[78:79], v[106:107], v[28:29], v[78:79] op_sel:[0,1,0] op_sel_hi:[0,0,1]
	s_waitcnt vmcnt(9)
	s_nop 0
	v_mov_b32_dpp v32, v36 row_shr:1 row_mask:0xf bank_mask:0xf
	v_mov_b32_dpp v33, v37 row_shr:1 row_mask:0xf bank_mask:0xf
	v_mov_b32_dpp v38, v34 row_shl:1 row_mask:0xf bank_mask:0xf
	v_mov_b32_dpp v39, v35 row_shl:1 row_mask:0xf bank_mask:0xf
	v_pk_mul_f32 v[34:35], v[34:35], s[32:33]
	v_pk_mul_f32 v[36:37], v[36:37], s[32:33]
	v_cndmask_b32_e64 v33, v33, v32, vcc
	v_cndmask_b32_e64 v38, v38, v39, s[16:17]
	v_pk_mul_f32 v[84:85], v[34:35], s[30:31]
	v_pk_mul_f32 v[86:87], v[36:37], s[30:31]
	v_pk_mul_f32 v[32:33], v[32:33], s[32:33]
	v_pk_mul_f32 v[38:39], v[38:39], s[32:33]
	s_cmp_eq_u32 s19, 0
	s_cbranch_scc1 .Lmyha4
	s_setprio 2
	s_branch .Lmyhb4

.Lmyhb4:
	s_nop 0
	v_pk_add_f32 v[96:97], v[34:35], v[16:17] neg_lo:[0,1] neg_hi:[0,1]
	v_pk_add_f32 v[98:99], v[32:33], v[18:19] neg_lo:[0,1] neg_hi:[0,1]
	v_pk_add_f32 v[100:101], v[34:35], v[18:19] neg_lo:[0,1] neg_hi:[0,1]
	v_pk_add_f32 v[102:103], v[36:37], v[18:19] neg_lo:[0,1] neg_hi:[0,1]
	v_pk_fma_f32 v[96:97], v[96:97], v[96:97], s[28:29] neg_lo:[1,0,0] neg_hi:[1,0,0]
	v_pk_fma_f32 v[98:99], v[98:99], v[98:99], s[28:29] neg_lo:[1,0,0] neg_hi:[1,0,0]
	v_pk_fma_f32 v[100:101], v[100:101], v[100:101], s[22:23] neg_lo:[1,0,0] neg_hi:[1,0,0]
	v_pk_fma_f32 v[102:103], v[102:103], v[102:103], s[28:29] neg_lo:[1,0,0] neg_hi:[1,0,0]
	v_exp_f32_e32 v96, v96
	v_exp_f32_e32 v97, v97
	v_exp_f32_e32 v98, v98
	v_exp_f32_e32 v99, v99
	v_exp_f32_e32 v100, v100
	v_exp_f32_e32 v101, v101
	v_exp_f32_e32 v102, v102
	v_exp_f32_e32 v103, v103
	v_pk_add_f32 v[104:105], v[34:35], v[20:21] neg_lo:[0,1] neg_hi:[0,1]
	v_pk_add_f32 v[106:107], v[36:37], v[20:21] neg_lo:[0,1] neg_hi:[0,1]
	v_pk_add_f32 v[108:109], v[38:39], v[20:21] neg_lo:[0,1] neg_hi:[0,1]
	v_pk_add_f32 v[110:111], v[36:37], v[22:23] neg_lo:[0,1] neg_hi:[0,1]
	v_pk_fma_f32 v[104:105], v[104:105], v[104:105], s[28:29] neg_lo:[1,0,0] neg_hi:[1,0,0]
	v_pk_fma_f32 v[106:107], v[106:107], v[106:107], s[22:23] neg_lo:[1,0,0] neg_hi:[1,0,0]
	v_pk_fma_f32 v[108:109], v[108:109], v[108:109], s[28:29] neg_lo:[1,0,0] neg_hi:[1,0,0]
	v_pk_fma_f32 v[110:111], v[110:111], v[110:111], s[28:29] neg_lo:[1,0,0] neg_hi:[1,0,0]
	v_exp_f32_e32 v104, v104
	v_exp_f32_e32 v105, v105
	v_exp_f32_e32 v106, v106
	v_exp_f32_e32 v107, v107
	v_exp_f32_e32 v108, v108
	v_exp_f32_e32 v109, v109
	v_exp_f32_e32 v110, v110
	v_exp_f32_e32 v111, v111
	v_pk_add_f32 v[80:81], s[30:31], v[96:97]
	v_pk_fma_f32 v[84:85], v[96:97], v[16:17], v[84:85]
	v_pk_add_f32 v[64:65], v[64:65], v[98:99]
	v_pk_fma_f32 v[68:69], v[98:99], v[32:33], v[68:69]
	v_pk_add_f32 v[80:81], v[80:81], v[100:101]
	v_pk_add_f32 v[64:65], v[64:65], v[100:101]
	v_pk_fma_f32 v[68:69], v[100:101], v[34:35], v[68:69]
	v_pk_fma_f32 v[84:85], v[100:101], v[18:19], v[84:85]
	v_pk_add_f32 v[64:65], v[64:65], v[102:103]
	v_pk_fma_f32 v[68:69], v[102:103], v[36:37], v[68:69]
	v_pk_add_f32 v[82:83], s[30:31], v[102:103]
	v_pk_fma_f32 v[86:87], v[102:103], v[18:19], v[86:87]
	v_pk_add_f32 v[96:97], v[34:35], v[18:19] op_sel:[1,0] op_sel_hi:[0,1] neg_lo:[0,1] neg_hi:[0,1]
	v_pk_add_f32 v[98:99], v[36:37], v[20:21] op_sel:[1,0] op_sel_hi:[0,1] neg_lo:[0,1] neg_hi:[0,1]
	v_pk_add_f32 v[100:101], v[34:35], v[24:25] neg_lo:[0,1] neg_hi:[0,1]
	v_pk_add_f32 v[102:103], v[32:33], v[26:27] neg_lo:[0,1] neg_hi:[0,1]
	v_pk_fma_f32 v[96:97], v[96:97], v[96:97], s[26:27] neg_lo:[1,0,0] neg_hi:[1,0,0]
	v_pk_fma_f32 v[98:99], v[98:99], v[98:99], s[26:27] neg_lo:[1,0,0] neg_hi:[1,0,0]
	v_pk_fma_f32 v[100:101], v[100:101], v[100:101], s[26:27] neg_lo:[1,0,0] neg_hi:[1,0,0]
	v_pk_fma_f32 v[102:103], v[102:103], v[102:103], s[26:27] neg_lo:[1,0,0] neg_hi:[1,0,0]
	v_exp_f32_e32 v96, v96
	v_exp_f32_e32 v97, v97
	v_exp_f32_e32 v98, v98
	v_exp_f32_e32 v99, v99
	v_exp_f32_e32 v100, v100
	v_exp_f32_e32 v101, v101
	v_exp_f32_e32 v102, v102
	v_exp_f32_e32 v103, v103
	v_pk_add_f32 v[66:67], v[66:67], v[104:105]
	v_pk_fma_f32 v[70:71], v[104:105], v[34:35], v[70:71]
	v_pk_add_f32 v[80:81], v[80:81], v[104:105]
	v_pk_fma_f32 v[84:85], v[104:105], v[20:21], v[84:85]
	v_pk_add_f32 v[66:67], v[66:67], v[106:107]
	v_pk_fma_f32 v[70:71], v[106:107], v[36:37], v[70:71]
	v_pk_add_f32 v[82:83], v[82:83], v[106:107]
	v_pk_fma_f32 v[86:87], v[106:107], v[20:21], v[86:87]
	v_pk_add_f32 v[66:67], v[66:67], v[108:109]
	v_pk_fma_f32 v[70:71], v[108:109], v[38:39], v[70:71]
	v_pk_add_f32 v[82:83], v[82:83], v[110:111]
	v_pk_fma_f32 v[86:87], v[110:111], v[22:23], v[86:87]
	v_pk_add_f32 v[104:105], v[34:35], v[26:27] neg_lo:[0,1] neg_hi:[0,1]
	v_pk_add_f32 v[106:107], v[36:37], v[26:27] neg_lo:[0,1] neg_hi:[0,1]
	v_pk_add_f32 v[108:109], v[34:35], v[28:29] neg_lo:[0,1] neg_hi:[0,1]
	v_pk_add_f32 v[110:111], v[36:37], v[28:29] neg_lo:[0,1] neg_hi:[0,1]
	v_pk_fma_f32 v[104:105], v[104:105], v[104:105], s[20:21] neg_lo:[1,0,0] neg_hi:[1,0,0]
	v_pk_fma_f32 v[106:107], v[106:107], v[106:107], s[26:27] neg_lo:[1,0,0] neg_hi:[1,0,0]
	v_pk_fma_f32 v[108:109], v[108:109], v[108:109], s[26:27] neg_lo:[1,0,0] neg_hi:[1,0,0]
	v_pk_fma_f32 v[110:111], v[110:111], v[110:111], s[20:21] neg_lo:[1,0,0] neg_hi:[1,0,0]
	v_exp_f32_e32 v104, v104
	v_exp_f32_e32 v105, v105
	v_exp_f32_e32 v106, v106
	v_exp_f32_e32 v107, v107
	v_exp_f32_e32 v108, v108
	v_exp_f32_e32 v109, v109
	v_exp_f32_e32 v110, v110
	v_exp_f32_e32 v111, v111
	v_pk_add_f32 v[64:65], v[64:65], v[96:97]
	v_pk_fma_f32 v[68:69], v[96:97], v[34:35], v[68:69] op_sel:[0,1,0] op_sel_hi:[1,0,1]
	v_pk_add_f32 v[80:81], v[80:81], v[96:97] op_sel:[0,1] op_sel_hi:[1,0]
	v_pk_fma_f32 v[84:85], v[96:97], v[18:19], v[84:85] op_sel:[1,1,0] op_sel_hi:[0,0,1]
	v_pk_add_f32 v[66:67], v[66:67], v[98:99]
	v_pk_fma_f32 v[70:71], v[98:99], v[36:37], v[70:71] op_sel:[0,1,0] op_sel_hi:[1,0,1]
	v_pk_add_f32 v[82:83], v[82:83], v[98:99] op_sel:[0,1] op_sel_hi:[1,0]
	v_pk_fma_f32 v[86:87], v[98:99], v[20:21], v[86:87] op_sel:[1,1,0] op_sel_hi:[0,0,1]
	v_pk_add_f32 v[80:81], v[80:81], v[100:101]
	v_pk_fma_f32 v[84:85], v[100:101], v[24:25], v[84:85]
	v_pk_add_f32 v[72:73], v[72:73], v[102:103]
	v_pk_fma_f32 v[76:77], v[102:103], v[32:33], v[76:77]
	v_pk_add_f32 v[96:97], v[38:39], v[28:29] neg_lo:[0,1] neg_hi:[0,1]
	v_pk_add_f32 v[98:99], v[36:37], v[30:31] neg_lo:[0,1] neg_hi:[0,1]
	v_pk_add_f32 v[100:101], v[34:35], v[26:27] op_sel:[1,0] op_sel_hi:[0,1] neg_lo:[0,1] neg_hi:[0,1]
	v_pk_add_f32 v[102:103], v[36:37], v[28:29] op_sel:[1,0] op_sel_hi:[0,1] neg_lo:[0,1] neg_hi:[0,1]
	v_pk_fma_f32 v[96:97], v[96:97], v[96:97], s[26:27] neg_lo:[1,0,0] neg_hi:[1,0,0]
	v_pk_fma_f32 v[98:99], v[98:99], v[98:99], s[26:27] neg_lo:[1,0,0] neg_hi:[1,0,0]
	v_pk_fma_f32 v[100:101], v[100:101], v[100:101], s[24:25] neg_lo:[1,0,0] neg_hi:[1,0,0]
	v_pk_fma_f32 v[102:103], v[102:103], v[102:103], s[24:25] neg_lo:[1,0,0] neg_hi:[1,0,0]
	v_exp_f32_e32 v96, v96
	v_exp_f32_e32 v97, v97
	v_exp_f32_e32 v98, v98
	v_exp_f32_e32 v99, v99
	v_exp_f32_e32 v100, v100
	v_exp_f32_e32 v101, v101
	v_exp_f32_e32 v102, v102
	v_exp_f32_e32 v103, v103
	v_pk_add_f32 v[72:73], v[72:73], v[104:105]
	v_pk_fma_f32 v[76:77], v[104:105], v[34:35], v[76:77]
	v_pk_add_f32 v[80:81], v[80:81], v[104:105]
	v_pk_fma_f32 v[84:85], v[104:105], v[26:27], v[84:85]
	v_pk_add_f32 v[72:73], v[72:73], v[106:107]
	v_pk_fma_f32 v[76:77], v[106:107], v[36:37], v[76:77]
	v_pk_add_f32 v[82:83], v[82:83], v[106:107]
	v_pk_fma_f32 v[86:87], v[106:107], v[26:27], v[86:87]
	v_pk_add_f32 v[74:75], v[74:75], v[108:109]
	v_pk_fma_f32 v[78:79], v[108:109], v[34:35], v[78:79]
	v_pk_add_f32 v[80:81], v[80:81], v[108:109]
	v_pk_fma_f32 v[84:85], v[108:109], v[28:29], v[84:85]
	v_pk_add_f32 v[74:75], v[74:75], v[110:111]
	v_pk_fma_f32 v[78:79], v[110:111], v[36:37], v[78:79]
	v_pk_add_f32 v[82:83], v[82:83], v[110:111]
	v_pk_fma_f32 v[86:87], v[110:111], v[28:29], v[86:87]
	v_pk_add_f32 v[104:105], v[34:35], v[32:33] neg_lo:[0,1] neg_hi:[0,1]
	v_pk_add_f32 v[106:107], v[36:37], v[34:35] neg_lo:[0,1] neg_hi:[0,1]
	v_pk_add_f32 v[108:109], v[38:39], v[36:37] neg_lo:[0,1] neg_hi:[0,1]
	v_pk_fma_f32 v[104:105], v[104:105], v[104:105], s[22:23] neg_lo:[1,0,0] neg_hi:[1,0,0]
	v_pk_fma_f32 v[106:107], v[106:107], v[106:107], s[22:23] neg_lo:[1,0,0] neg_hi:[1,0,0]
	v_pk_fma_f32 v[108:109], v[108:109], v[108:109], s[22:23] neg_lo:[1,0,0] neg_hi:[1,0,0]
	v_exp_f32_e32 v104, v104
	v_exp_f32_e32 v105, v105
	v_exp_f32_e32 v106, v106
	v_exp_f32_e32 v107, v107
	v_exp_f32_e32 v108, v108
	v_exp_f32_e32 v109, v109
	v_pk_add_f32 v[74:75], v[74:75], v[96:97]
	v_pk_fma_f32 v[78:79], v[96:97], v[38:39], v[78:79]
	v_pk_add_f32 v[82:83], v[82:83], v[98:99]
	v_pk_fma_f32 v[86:87], v[98:99], v[30:31], v[86:87]
	v_pk_add_f32 v[72:73], v[72:73], v[100:101]
	v_pk_fma_f32 v[76:77], v[100:101], v[34:35], v[76:77] op_sel:[0,1,0] op_sel_hi:[1,0,1]
	v_pk_add_f32 v[80:81], v[80:81], v[100:101] op_sel:[0,1] op_sel_hi:[1,0]
	v_pk_fma_f32 v[84:85], v[100:101], v[26:27], v[84:85] op_sel:[1,1,0] op_sel_hi:[0,0,1]
	v_pk_add_f32 v[74:75], v[74:75], v[102:103]
	v_pk_fma_f32 v[78:79], v[102:103], v[36:37], v[78:79] op_sel:[0,1,0] op_sel_hi:[1,0,1]
	v_pk_add_f32 v[82:83], v[82:83], v[102:103] op_sel:[0,1] op_sel_hi:[1,0]
	v_pk_fma_f32 v[86:87], v[102:103], v[28:29], v[86:87] op_sel:[1,1,0] op_sel_hi:[0,0,1]
	v_sub_f32_e32 v96, v34, v17
	v_sub_f32_e32 v98, v33, v18
	v_sub_f32_e32 v100, v36, v19
	v_sub_f32_e32 v102, v35, v20
	v_sub_f32_e32 v97, v38, v21
	v_sub_f32_e32 v99, v37, v22
	v_sub_f32_e32 v101, v34, v25
	v_sub_f32_e32 v103, v33, v26
	v_fma_f32 v96, -v96, v96, s26
	v_fma_f32 v98, -v98, v98, s26
	v_fma_f32 v100, -v100, v100, s26
	v_fma_f32 v102, -v102, v102, s26
	v_fma_f32 v97, -v97, v97, s26
	v_fma_f32 v99, -v99, v99, s26
	v_fma_f32 v101, -v101, v101, s24
	v_fma_f32 v103, -v103, v103, s24
	v_exp_f32_e32 v96, v96
	v_exp_f32_e32 v98, v98
	v_exp_f32_e32 v100, v100
	v_exp_f32_e32 v102, v102
	v_exp_f32_e32 v97, v97
	v_exp_f32_e32 v99, v99
	v_exp_f32_e32 v101, v101
	v_exp_f32_e32 v103, v103
	v_pk_add_f32 v[80:81], v[80:81], v[104:105]
	v_pk_fma_f32 v[84:85], v[104:105], v[32:33], v[84:85]
	v_pk_add_f32 v[82:83], v[82:83], v[106:107]
	v_pk_add_f32 v[80:81], v[80:81], v[106:107]
	v_pk_fma_f32 v[84:85], v[106:107], v[36:37], v[84:85]
	v_pk_fma_f32 v[86:87], v[106:107], v[34:35], v[86:87]
	v_pk_add_f32 v[82:83], v[82:83], v[108:109]
	v_pk_fma_f32 v[86:87], v[108:109], v[38:39], v[86:87]
	v_sub_f32_e32 v108, v36, v27
	v_sub_f32_e32 v110, v35, v28
	v_sub_f32_e32 v105, v38, v29
	v_sub_f32_e32 v107, v37, v30
	v_sub_f32_e32 v109, v34, v33
	v_sub_f32_e32 v104, v35, v34
	v_sub_f32_e32 v111, v36, v35
	v_sub_f32_e32 v106, v37, v36
	v_fma_f32 v108, -v108, v108, s24
	v_fma_f32 v110, -v110, v110, s24
	v_fma_f32 v105, -v105, v105, s24
	v_fma_f32 v107, -v107, v107, s24
	v_fma_f32 v109, -v109, v109, s20
	v_fma_f32 v104, -v104, v104, s20
	v_fma_f32 v111, -v111, v111, s20
	v_fma_f32 v106, -v106, v106, s20
	v_exp_f32_e32 v108, v108
	v_exp_f32_e32 v110, v110
	v_exp_f32_e32 v105, v105
	v_exp_f32_e32 v107, v107
	v_exp_f32_e32 v109, v109
	v_exp_f32_e32 v104, v104
	v_exp_f32_e32 v111, v111
	v_exp_f32_e32 v106, v106
	v_add_f32_e32 v80, v80, v96
	v_fmac_f32_e32 v84, v96, v17
	v_add_f32_e32 v64, v64, v98
	v_fmac_f32_e32 v68, v98, v33
	v_add_f32_e32 v65, v65, v100
	v_fmac_f32_e32 v69, v100, v36
	v_add_f32_e32 v82, v82, v100
	v_fmac_f32_e32 v86, v100, v19
	v_add_f32_e32 v66, v66, v102
	v_fmac_f32_e32 v70, v102, v35
	v_add_f32_e32 v81, v81, v102
	v_fmac_f32_e32 v85, v102, v20
	v_add_f32_e32 v67, v67, v97
	v_fmac_f32_e32 v71, v97, v38
	v_add_f32_e32 v83, v83, v99
	v_fmac_f32_e32 v87, v99, v22
	v_add_f32_e32 v80, v80, v101
	v_fmac_f32_e32 v84, v101, v25
	v_add_f32_e32 v72, v72, v103
	v_fmac_f32_e32 v76, v103, v33
	v_sub_f32_e64 v96, v38, v37
	v_fma_f32 v96, -v96, v96, s20
	s_nop 0
	v_exp_f32_e32 v96, v96
	v_add_f32_e32 v73, v73, v108
	v_fmac_f32_e32 v77, v108, v36
	v_add_f32_e32 v82, v82, v108
	v_fmac_f32_e32 v86, v108, v27
	v_add_f32_e32 v74, v74, v110
	v_fmac_f32_e32 v78, v110, v35
	v_add_f32_e32 v81, v81, v110
	v_fmac_f32_e32 v85, v110, v28
	v_add_f32_e32 v75, v75, v105
	v_fmac_f32_e32 v79, v105, v38
	v_add_f32_e32 v83, v83, v107
	v_fmac_f32_e32 v87, v107, v30
	v_add_f32_e32 v80, v80, v109
	v_fmac_f32_e32 v84, v109, v33
	v_add_f32_e32 v81, v81, v111
	v_fmac_f32_e32 v85, v111, v36
	v_add_f32_e32 v82, v82, v111
	v_fmac_f32_e32 v86, v111, v35
	v_pk_add_f32 v[80:81], v[80:81], v[104:105] op_sel_hi:[1,0]
	v_pk_fma_f32 v[84:85], v[104:105], v[34:35], v[84:85] op_sel:[0,1,0] op_sel_hi:[0,0,1]
	v_pk_add_f32 v[82:83], v[82:83], v[106:107] op_sel_hi:[1,0]
	v_pk_fma_f32 v[86:87], v[106:107], v[36:37], v[86:87] op_sel:[0,1,0] op_sel_hi:[0,0,1]
	s_nop 0
	v_add_f32_e32 v83, v83, v96
	v_fmac_f32_e32 v87, v96, v38
	v_rcp_f32_e32 v96, v64
	v_rcp_f32_e32 v97, v65
	v_rcp_f32_e32 v98, v66
	v_rcp_f32_e64 v99, v67
	v_pk_mul_f32 v[68:69], v[68:69], s[34:35]
	v_pk_mul_f32 v[70:71], v[70:71], s[34:35]
	v_pk_mul_f32 v[68:69], v[68:69], v[96:97]
	v_pk_mul_f32 v[70:71], v[70:71], v[98:99]
	buffer_store_dwordx4 v[68:71], v114, s[12:15], 0 offen sc1
	s_waitcnt vmcnt(7)
	s_nop 0
	v_mov_b32_dpp v40, v44 row_shr:1 row_mask:0xf bank_mask:0xf
	v_mov_b32_dpp v41, v45 row_shr:1 row_mask:0xf bank_mask:0xf
	v_mov_b32_dpp v46, v42 row_shl:1 row_mask:0xf bank_mask:0xf
	v_mov_b32_dpp v47, v43 row_shl:1 row_mask:0xf bank_mask:0xf
	v_pk_mul_f32 v[42:43], v[42:43], s[32:33]
	v_pk_mul_f32 v[44:45], v[44:45], s[32:33]
	v_cndmask_b32_e64 v41, v41, v40, vcc
	v_cndmask_b32_e64 v46, v46, v47, s[16:17]
	v_pk_mul_f32 v[92:93], v[42:43], s[30:31]
	v_pk_mul_f32 v[94:95], v[44:45], s[30:31]
	v_pk_mul_f32 v[40:41], v[40:41], s[32:33]
	v_pk_mul_f32 v[46:47], v[46:47], s[32:33]
	s_cmp_eq_u32 s19, 0
	s_cbranch_scc1 .Lmyha5
	s_setprio 1
	s_branch .Lmyhb5

.Lmyhb5:
	s_nop 0
	v_pk_add_f32 v[96:97], v[42:43], v[24:25] neg_lo:[0,1] neg_hi:[0,1]
	v_pk_add_f32 v[98:99], v[40:41], v[26:27] neg_lo:[0,1] neg_hi:[0,1]
	v_pk_add_f32 v[100:101], v[42:43], v[26:27] neg_lo:[0,1] neg_hi:[0,1]
	v_pk_add_f32 v[102:103], v[44:45], v[26:27] neg_lo:[0,1] neg_hi:[0,1]
	v_pk_fma_f32 v[96:97], v[96:97], v[96:97], s[28:29] neg_lo:[1,0,0] neg_hi:[1,0,0]
	v_pk_fma_f32 v[98:99], v[98:99], v[98:99], s[28:29] neg_lo:[1,0,0] neg_hi:[1,0,0]
	v_pk_fma_f32 v[100:101], v[100:101], v[100:101], s[22:23] neg_lo:[1,0,0] neg_hi:[1,0,0]
	v_pk_fma_f32 v[102:103], v[102:103], v[102:103], s[28:29] neg_lo:[1,0,0] neg_hi:[1,0,0]
	v_exp_f32_e32 v96, v96
	v_exp_f32_e32 v97, v97
	v_exp_f32_e32 v98, v98
	v_exp_f32_e32 v99, v99
	v_exp_f32_e32 v100, v100
	v_exp_f32_e32 v101, v101
	v_exp_f32_e32 v102, v102
	v_exp_f32_e32 v103, v103
	v_pk_add_f32 v[104:105], v[42:43], v[28:29] neg_lo:[0,1] neg_hi:[0,1]
	v_pk_add_f32 v[106:107], v[44:45], v[28:29] neg_lo:[0,1] neg_hi:[0,1]
	v_pk_add_f32 v[108:109], v[46:47], v[28:29] neg_lo:[0,1] neg_hi:[0,1]
	v_pk_add_f32 v[110:111], v[44:45], v[30:31] neg_lo:[0,1] neg_hi:[0,1]
	v_pk_fma_f32 v[104:105], v[104:105], v[104:105], s[28:29] neg_lo:[1,0,0] neg_hi:[1,0,0]
	v_pk_fma_f32 v[106:107], v[106:107], v[106:107], s[22:23] neg_lo:[1,0,0] neg_hi:[1,0,0]
	v_pk_fma_f32 v[108:109], v[108:109], v[108:109], s[28:29] neg_lo:[1,0,0] neg_hi:[1,0,0]
	v_pk_fma_f32 v[110:111], v[110:111], v[110:111], s[28:29] neg_lo:[1,0,0] neg_hi:[1,0,0]
	v_exp_f32_e32 v104, v104
	v_exp_f32_e32 v105, v105
	v_exp_f32_e32 v106, v106
	v_exp_f32_e32 v107, v107
	v_exp_f32_e32 v108, v108
	v_exp_f32_e32 v109, v109
	v_exp_f32_e32 v110, v110
	v_exp_f32_e32 v111, v111
	v_pk_add_f32 v[88:89], s[30:31], v[96:97]
	v_pk_fma_f32 v[92:93], v[96:97], v[24:25], v[92:93]
	v_pk_add_f32 v[72:73], v[72:73], v[98:99]
	v_pk_fma_f32 v[76:77], v[98:99], v[40:41], v[76:77]
	v_pk_add_f32 v[88:89], v[88:89], v[100:101]
	v_pk_add_f32 v[72:73], v[72:73], v[100:101]
	v_pk_fma_f32 v[76:77], v[100:101], v[42:43], v[76:77]
	v_pk_fma_f32 v[92:93], v[100:101], v[26:27], v[92:93]
	v_pk_add_f32 v[72:73], v[72:73], v[102:103]
	v_pk_fma_f32 v[76:77], v[102:103], v[44:45], v[76:77]
	v_pk_add_f32 v[90:91], s[30:31], v[102:103]
	v_pk_fma_f32 v[94:95], v[102:103], v[26:27], v[94:95]
	v_pk_add_f32 v[96:97], v[42:43], v[26:27] op_sel:[1,0] op_sel_hi:[0,1] neg_lo:[0,1] neg_hi:[0,1]
	v_pk_add_f32 v[98:99], v[44:45], v[28:29] op_sel:[1,0] op_sel_hi:[0,1] neg_lo:[0,1] neg_hi:[0,1]
	v_pk_add_f32 v[100:101], v[42:43], v[32:33] neg_lo:[0,1] neg_hi:[0,1]
	v_pk_add_f32 v[102:103], v[40:41], v[34:35] neg_lo:[0,1] neg_hi:[0,1]
	v_pk_fma_f32 v[96:97], v[96:97], v[96:97], s[26:27] neg_lo:[1,0,0] neg_hi:[1,0,0]
	v_pk_fma_f32 v[98:99], v[98:99], v[98:99], s[26:27] neg_lo:[1,0,0] neg_hi:[1,0,0]
	v_pk_fma_f32 v[100:101], v[100:101], v[100:101], s[26:27] neg_lo:[1,0,0] neg_hi:[1,0,0]
	v_pk_fma_f32 v[102:103], v[102:103], v[102:103], s[26:27] neg_lo:[1,0,0] neg_hi:[1,0,0]
	v_exp_f32_e32 v96, v96
	v_exp_f32_e32 v97, v97
	v_exp_f32_e32 v98, v98
	v_exp_f32_e32 v99, v99
	v_exp_f32_e32 v100, v100
	v_exp_f32_e32 v101, v101
	v_exp_f32_e32 v102, v102
	v_exp_f32_e32 v103, v103
	v_pk_add_f32 v[74:75], v[74:75], v[104:105]
	v_pk_fma_f32 v[78:79], v[104:105], v[42:43], v[78:79]
	v_pk_add_f32 v[88:89], v[88:89], v[104:105]
	v_pk_fma_f32 v[92:93], v[104:105], v[28:29], v[92:93]
	v_pk_add_f32 v[74:75], v[74:75], v[106:107]
	v_pk_fma_f32 v[78:79], v[106:107], v[44:45], v[78:79]
	v_pk_add_f32 v[90:91], v[90:91], v[106:107]
	v_pk_fma_f32 v[94:95], v[106:107], v[28:29], v[94:95]
	v_pk_add_f32 v[74:75], v[74:75], v[108:109]
	v_pk_fma_f32 v[78:79], v[108:109], v[46:47], v[78:79]
	v_pk_add_f32 v[90:91], v[90:91], v[110:111]
	v_pk_fma_f32 v[94:95], v[110:111], v[30:31], v[94:95]
	v_pk_add_f32 v[104:105], v[42:43], v[34:35] neg_lo:[0,1] neg_hi:[0,1]
	v_pk_add_f32 v[106:107], v[44:45], v[34:35] neg_lo:[0,1] neg_hi:[0,1]
	v_pk_add_f32 v[108:109], v[42:43], v[36:37] neg_lo:[0,1] neg_hi:[0,1]
	v_pk_add_f32 v[110:111], v[44:45], v[36:37] neg_lo:[0,1] neg_hi:[0,1]
	v_pk_fma_f32 v[104:105], v[104:105], v[104:105], s[20:21] neg_lo:[1,0,0] neg_hi:[1,0,0]
	v_pk_fma_f32 v[106:107], v[106:107], v[106:107], s[26:27] neg_lo:[1,0,0] neg_hi:[1,0,0]
	v_pk_fma_f32 v[108:109], v[108:109], v[108:109], s[26:27] neg_lo:[1,0,0] neg_hi:[1,0,0]
	v_pk_fma_f32 v[110:111], v[110:111], v[110:111], s[20:21] neg_lo:[1,0,0] neg_hi:[1,0,0]
	v_exp_f32_e32 v104, v104
	v_exp_f32_e32 v105, v105
	v_exp_f32_e32 v106, v106
	v_exp_f32_e32 v107, v107
	v_exp_f32_e32 v108, v108
	v_exp_f32_e32 v109, v109
	v_exp_f32_e32 v110, v110
	v_exp_f32_e32 v111, v111
	v_pk_add_f32 v[72:73], v[72:73], v[96:97]
	v_pk_fma_f32 v[76:77], v[96:97], v[42:43], v[76:77] op_sel:[0,1,0] op_sel_hi:[1,0,1]
	v_pk_add_f32 v[88:89], v[88:89], v[96:97] op_sel:[0,1] op_sel_hi:[1,0]
	v_pk_fma_f32 v[92:93], v[96:97], v[26:27], v[92:93] op_sel:[1,1,0] op_sel_hi:[0,0,1]
	v_pk_add_f32 v[74:75], v[74:75], v[98:99]
	v_pk_fma_f32 v[78:79], v[98:99], v[44:45], v[78:79] op_sel:[0,1,0] op_sel_hi:[1,0,1]
	v_pk_add_f32 v[90:91], v[90:91], v[98:99] op_sel:[0,1] op_sel_hi:[1,0]
	v_pk_fma_f32 v[94:95], v[98:99], v[28:29], v[94:95] op_sel:[1,1,0] op_sel_hi:[0,0,1]
	v_pk_add_f32 v[88:89], v[88:89], v[100:101]
	v_pk_fma_f32 v[92:93], v[100:101], v[32:33], v[92:93]
	v_pk_add_f32 v[80:81], v[80:81], v[102:103]
	v_pk_fma_f32 v[84:85], v[102:103], v[40:41], v[84:85]
	v_pk_add_f32 v[96:97], v[46:47], v[36:37] neg_lo:[0,1] neg_hi:[0,1]
	v_pk_add_f32 v[98:99], v[44:45], v[38:39] neg_lo:[0,1] neg_hi:[0,1]
	v_pk_add_f32 v[100:101], v[42:43], v[34:35] op_sel:[1,0] op_sel_hi:[0,1] neg_lo:[0,1] neg_hi:[0,1]
	v_pk_add_f32 v[102:103], v[44:45], v[36:37] op_sel:[1,0] op_sel_hi:[0,1] neg_lo:[0,1] neg_hi:[0,1]
	v_pk_fma_f32 v[96:97], v[96:97], v[96:97], s[26:27] neg_lo:[1,0,0] neg_hi:[1,0,0]
	v_pk_fma_f32 v[98:99], v[98:99], v[98:99], s[26:27] neg_lo:[1,0,0] neg_hi:[1,0,0]
	v_pk_fma_f32 v[100:101], v[100:101], v[100:101], s[24:25] neg_lo:[1,0,0] neg_hi:[1,0,0]
	v_pk_fma_f32 v[102:103], v[102:103], v[102:103], s[24:25] neg_lo:[1,0,0] neg_hi:[1,0,0]
	v_exp_f32_e32 v96, v96
	v_exp_f32_e32 v97, v97
	v_exp_f32_e32 v98, v98
	v_exp_f32_e32 v99, v99
	v_exp_f32_e32 v100, v100
	v_exp_f32_e32 v101, v101
	v_exp_f32_e32 v102, v102
	v_exp_f32_e32 v103, v103
	v_pk_add_f32 v[80:81], v[80:81], v[104:105]
	v_pk_fma_f32 v[84:85], v[104:105], v[42:43], v[84:85]
	v_pk_add_f32 v[88:89], v[88:89], v[104:105]
	v_pk_fma_f32 v[92:93], v[104:105], v[34:35], v[92:93]
	v_pk_add_f32 v[80:81], v[80:81], v[106:107]
	v_pk_fma_f32 v[84:85], v[106:107], v[44:45], v[84:85]
	v_pk_add_f32 v[90:91], v[90:91], v[106:107]
	v_pk_fma_f32 v[94:95], v[106:107], v[34:35], v[94:95]
	v_pk_add_f32 v[82:83], v[82:83], v[108:109]
	v_pk_fma_f32 v[86:87], v[108:109], v[42:43], v[86:87]
	v_pk_add_f32 v[88:89], v[88:89], v[108:109]
	v_pk_fma_f32 v[92:93], v[108:109], v[36:37], v[92:93]
	v_pk_add_f32 v[82:83], v[82:83], v[110:111]
	v_pk_fma_f32 v[86:87], v[110:111], v[44:45], v[86:87]
	v_pk_add_f32 v[90:91], v[90:91], v[110:111]
	v_pk_fma_f32 v[94:95], v[110:111], v[36:37], v[94:95]
	v_pk_add_f32 v[104:105], v[42:43], v[40:41] neg_lo:[0,1] neg_hi:[0,1]
	v_pk_add_f32 v[106:107], v[44:45], v[42:43] neg_lo:[0,1] neg_hi:[0,1]
	v_pk_add_f32 v[108:109], v[46:47], v[44:45] neg_lo:[0,1] neg_hi:[0,1]
	v_pk_fma_f32 v[104:105], v[104:105], v[104:105], s[22:23] neg_lo:[1,0,0] neg_hi:[1,0,0]
	v_pk_fma_f32 v[106:107], v[106:107], v[106:107], s[22:23] neg_lo:[1,0,0] neg_hi:[1,0,0]
	v_pk_fma_f32 v[108:109], v[108:109], v[108:109], s[22:23] neg_lo:[1,0,0] neg_hi:[1,0,0]
	v_exp_f32_e32 v104, v104
	v_exp_f32_e32 v105, v105
	v_exp_f32_e32 v106, v106
	v_exp_f32_e32 v107, v107
	v_exp_f32_e32 v108, v108
	v_exp_f32_e32 v109, v109
	v_pk_add_f32 v[82:83], v[82:83], v[96:97]
	v_pk_fma_f32 v[86:87], v[96:97], v[46:47], v[86:87]
	v_pk_add_f32 v[90:91], v[90:91], v[98:99]
	v_pk_fma_f32 v[94:95], v[98:99], v[38:39], v[94:95]
	v_pk_add_f32 v[80:81], v[80:81], v[100:101]
	v_pk_fma_f32 v[84:85], v[100:101], v[42:43], v[84:85] op_sel:[0,1,0] op_sel_hi:[1,0,1]
	v_pk_add_f32 v[88:89], v[88:89], v[100:101] op_sel:[0,1] op_sel_hi:[1,0]
	v_pk_fma_f32 v[92:93], v[100:101], v[34:35], v[92:93] op_sel:[1,1,0] op_sel_hi:[0,0,1]
	v_pk_add_f32 v[82:83], v[82:83], v[102:103]
	v_pk_fma_f32 v[86:87], v[102:103], v[44:45], v[86:87] op_sel:[0,1,0] op_sel_hi:[1,0,1]
	v_pk_add_f32 v[90:91], v[90:91], v[102:103] op_sel:[0,1] op_sel_hi:[1,0]
	v_pk_fma_f32 v[94:95], v[102:103], v[36:37], v[94:95] op_sel:[1,1,0] op_sel_hi:[0,0,1]
	v_sub_f32_e32 v96, v42, v25
	v_sub_f32_e32 v98, v41, v26
	v_sub_f32_e32 v100, v44, v27
	v_sub_f32_e32 v102, v43, v28
	v_sub_f32_e32 v97, v46, v29
	v_sub_f32_e32 v99, v45, v30
	v_sub_f32_e32 v101, v42, v33
	v_sub_f32_e32 v103, v41, v34
	v_fma_f32 v96, -v96, v96, s26
	v_fma_f32 v98, -v98, v98, s26
	v_fma_f32 v100, -v100, v100, s26
	v_fma_f32 v102, -v102, v102, s26
	v_fma_f32 v97, -v97, v97, s26
	v_fma_f32 v99, -v99, v99, s26
	v_fma_f32 v101, -v101, v101, s24
	v_fma_f32 v103, -v103, v103, s24
	v_exp_f32_e32 v96, v96
	v_exp_f32_e32 v98, v98
	v_exp_f32_e32 v100, v100
	v_exp_f32_e32 v102, v102
	v_exp_f32_e32 v97, v97
	v_exp_f32_e32 v99, v99
	v_exp_f32_e32 v101, v101
	v_exp_f32_e32 v103, v103
	v_pk_add_f32 v[88:89], v[88:89], v[104:105]
	v_pk_fma_f32 v[92:93], v[104:105], v[40:41], v[92:93]
	v_pk_add_f32 v[90:91], v[90:91], v[106:107]
	v_pk_add_f32 v[88:89], v[88:89], v[106:107]
	v_pk_fma_f32 v[92:93], v[106:107], v[44:45], v[92:93]
	v_pk_fma_f32 v[94:95], v[106:107], v[42:43], v[94:95]
	v_pk_add_f32 v[90:91], v[90:91], v[108:109]
	v_pk_fma_f32 v[94:95], v[108:109], v[46:47], v[94:95]
	v_sub_f32_e32 v108, v44, v35
	v_sub_f32_e32 v110, v43, v36
	v_sub_f32_e32 v105, v46, v37
	v_sub_f32_e32 v107, v45, v38
	v_sub_f32_e32 v109, v42, v41
	v_sub_f32_e32 v104, v43, v42
	v_sub_f32_e32 v111, v44, v43
	v_sub_f32_e32 v106, v45, v44
	v_fma_f32 v108, -v108, v108, s24
	v_fma_f32 v110, -v110, v110, s24
	v_fma_f32 v105, -v105, v105, s24
	v_fma_f32 v107, -v107, v107, s24
	v_fma_f32 v109, -v109, v109, s20
	v_fma_f32 v104, -v104, v104, s20
	v_fma_f32 v111, -v111, v111, s20
	v_fma_f32 v106, -v106, v106, s20
	v_exp_f32_e32 v108, v108
	v_exp_f32_e32 v110, v110
	v_exp_f32_e32 v105, v105
	v_exp_f32_e32 v107, v107
	v_exp_f32_e32 v109, v109
	v_exp_f32_e32 v104, v104
	v_exp_f32_e32 v111, v111
	v_exp_f32_e32 v106, v106
	v_add_f32_e32 v88, v88, v96
	v_fmac_f32_e32 v92, v96, v25
	v_add_f32_e32 v72, v72, v98
	v_fmac_f32_e32 v76, v98, v41
	v_add_f32_e32 v73, v73, v100
	v_fmac_f32_e32 v77, v100, v44
	v_add_f32_e32 v90, v90, v100
	v_fmac_f32_e32 v94, v100, v27
	v_add_f32_e32 v74, v74, v102
	v_fmac_f32_e32 v78, v102, v43
	v_add_f32_e32 v89, v89, v102
	v_fmac_f32_e32 v93, v102, v28
	v_add_f32_e32 v75, v75, v97
	v_fmac_f32_e32 v79, v97, v46
	v_add_f32_e32 v91, v91, v99
	v_fmac_f32_e32 v95, v99, v30
	v_add_f32_e32 v88, v88, v101
	v_fmac_f32_e32 v92, v101, v33
	v_add_f32_e32 v80, v80, v103
	v_fmac_f32_e32 v84, v103, v41
	v_sub_f32_e64 v96, v46, v45
	v_fma_f32 v96, -v96, v96, s20
	s_nop 0
	v_exp_f32_e32 v96, v96
	v_add_f32_e32 v81, v81, v108
	v_fmac_f32_e32 v85, v108, v44
	v_add_f32_e32 v90, v90, v108
	v_fmac_f32_e32 v94, v108, v35
	v_add_f32_e32 v82, v82, v110
	v_fmac_f32_e32 v86, v110, v43
	v_add_f32_e32 v89, v89, v110
	v_fmac_f32_e32 v93, v110, v36
	v_add_f32_e32 v83, v83, v105
	v_fmac_f32_e32 v87, v105, v46
	v_add_f32_e32 v91, v91, v107
	v_fmac_f32_e32 v95, v107, v38
	v_add_f32_e32 v88, v88, v109
	v_fmac_f32_e32 v92, v109, v41
	v_add_f32_e32 v89, v89, v111
	v_fmac_f32_e32 v93, v111, v44
	v_add_f32_e32 v90, v90, v111
	v_fmac_f32_e32 v94, v111, v43
	v_pk_add_f32 v[88:89], v[88:89], v[104:105] op_sel_hi:[1,0]
	v_pk_fma_f32 v[92:93], v[104:105], v[42:43], v[92:93] op_sel:[0,1,0] op_sel_hi:[0,0,1]
	v_pk_add_f32 v[90:91], v[90:91], v[106:107] op_sel_hi:[1,0]
	v_pk_fma_f32 v[94:95], v[106:107], v[44:45], v[94:95] op_sel:[0,1,0] op_sel_hi:[0,0,1]
	s_nop 0
	v_add_f32_e32 v91, v91, v96
	v_fmac_f32_e32 v95, v96, v46
	v_rcp_f32_e32 v96, v72
	v_rcp_f32_e32 v97, v73
	v_rcp_f32_e32 v98, v74
	v_rcp_f32_e64 v99, v75
	v_pk_mul_f32 v[76:77], v[76:77], s[34:35]
	v_pk_mul_f32 v[78:79], v[78:79], s[34:35]
	v_pk_mul_f32 v[76:77], v[76:77], v[96:97]
	v_pk_mul_f32 v[78:79], v[78:79], v[98:99]
	buffer_store_dwordx4 v[76:79], v114, s[12:15], 0 offen offset:2048 sc1
	s_waitcnt vmcnt(5)
	s_nop 0
	v_mov_b32_dpp v48, v52 row_shr:1 row_mask:0xf bank_mask:0xf
	v_mov_b32_dpp v49, v53 row_shr:1 row_mask:0xf bank_mask:0xf
	v_mov_b32_dpp v54, v50 row_shl:1 row_mask:0xf bank_mask:0xf
	v_mov_b32_dpp v55, v51 row_shl:1 row_mask:0xf bank_mask:0xf
	v_pk_mul_f32 v[50:51], v[50:51], s[32:33]
	v_pk_mul_f32 v[52:53], v[52:53], s[32:33]
	v_cndmask_b32_e64 v49, v49, v48, vcc
	v_cndmask_b32_e64 v54, v54, v55, s[16:17]
	v_pk_mul_f32 v[48:49], v[48:49], s[32:33]
	v_pk_mul_f32 v[54:55], v[54:55], s[32:33]
	s_cmp_eq_u32 s19, 0
	s_cbranch_scc1 .Lmyha6
	s_setprio 0
	s_branch .Lmyhb6

.Lmyhb6:
	s_nop 0
	v_pk_add_f32 v[96:97], v[48:49], v[34:35] neg_lo:[0,1] neg_hi:[0,1]
	v_pk_add_f32 v[98:99], v[50:51], v[34:35] neg_lo:[0,1] neg_hi:[0,1]
	v_pk_add_f32 v[100:101], v[52:53], v[34:35] neg_lo:[0,1] neg_hi:[0,1]
	v_pk_add_f32 v[102:103], v[50:51], v[36:37] neg_lo:[0,1] neg_hi:[0,1]
	v_pk_fma_f32 v[96:97], v[96:97], v[96:97], s[28:29] neg_lo:[1,0,0] neg_hi:[1,0,0]
	v_pk_fma_f32 v[98:99], v[98:99], v[98:99], s[22:23] neg_lo:[1,0,0] neg_hi:[1,0,0]
	v_pk_fma_f32 v[100:101], v[100:101], v[100:101], s[28:29] neg_lo:[1,0,0] neg_hi:[1,0,0]
	v_pk_fma_f32 v[102:103], v[102:103], v[102:103], s[28:29] neg_lo:[1,0,0] neg_hi:[1,0,0]
	v_exp_f32_e32 v96, v96
	v_exp_f32_e32 v97, v97
	v_exp_f32_e32 v98, v98
	v_exp_f32_e32 v99, v99
	v_exp_f32_e32 v100, v100
	v_exp_f32_e32 v101, v101
	v_exp_f32_e32 v102, v102
	v_exp_f32_e32 v103, v103
	v_pk_add_f32 v[104:105], v[52:53], v[36:37] neg_lo:[0,1] neg_hi:[0,1]
	v_pk_add_f32 v[106:107], v[54:55], v[36:37] neg_lo:[0,1] neg_hi:[0,1]
	v_pk_add_f32 v[108:109], v[50:51], v[34:35] op_sel:[1,0] op_sel_hi:[0,1] neg_lo:[0,1] neg_hi:[0,1]
	v_pk_add_f32 v[110:111], v[52:53], v[36:37] op_sel:[1,0] op_sel_hi:[0,1] neg_lo:[0,1] neg_hi:[0,1]
	v_pk_fma_f32 v[104:105], v[104:105], v[104:105], s[22:23] neg_lo:[1,0,0] neg_hi:[1,0,0]
	v_pk_fma_f32 v[106:107], v[106:107], v[106:107], s[28:29] neg_lo:[1,0,0] neg_hi:[1,0,0]
	v_pk_fma_f32 v[108:109], v[108:109], v[108:109], s[26:27] neg_lo:[1,0,0] neg_hi:[1,0,0]
	v_pk_fma_f32 v[110:111], v[110:111], v[110:111], s[26:27] neg_lo:[1,0,0] neg_hi:[1,0,0]
	v_exp_f32_e32 v104, v104
	v_exp_f32_e32 v105, v105
	v_exp_f32_e32 v106, v106
	v_exp_f32_e32 v107, v107
	v_exp_f32_e32 v108, v108
	v_exp_f32_e32 v109, v109
	v_exp_f32_e32 v110, v110
	v_exp_f32_e32 v111, v111
	v_pk_add_f32 v[80:81], v[80:81], v[96:97]
	v_pk_fma_f32 v[84:85], v[96:97], v[48:49], v[84:85]
	v_pk_add_f32 v[82:83], v[82:83], v[102:103]
	v_pk_add_f32 v[80:81], v[80:81], v[98:99]
	v_pk_fma_f32 v[84:85], v[98:99], v[50:51], v[84:85]
	v_pk_fma_f32 v[86:87], v[102:103], v[50:51], v[86:87]
	v_pk_add_f32 v[80:81], v[80:81], v[100:101]
	v_pk_fma_f32 v[84:85], v[100:101], v[52:53], v[84:85]
	v_pk_add_f32 v[96:97], v[48:49], v[42:43] neg_lo:[0,1] neg_hi:[0,1]
	v_pk_add_f32 v[98:99], v[50:51], v[42:43] neg_lo:[0,1] neg_hi:[0,1]
	v_pk_add_f32 v[100:101], v[52:53], v[42:43] neg_lo:[0,1] neg_hi:[0,1]
	v_pk_add_f32 v[102:103], v[50:51], v[44:45] neg_lo:[0,1] neg_hi:[0,1]
	v_pk_fma_f32 v[96:97], v[96:97], v[96:97], s[26:27] neg_lo:[1,0,0] neg_hi:[1,0,0]
	v_pk_fma_f32 v[98:99], v[98:99], v[98:99], s[20:21] neg_lo:[1,0,0] neg_hi:[1,0,0]
	v_pk_fma_f32 v[100:101], v[100:101], v[100:101], s[26:27] neg_lo:[1,0,0] neg_hi:[1,0,0]
	v_pk_fma_f32 v[102:103], v[102:103], v[102:103], s[26:27] neg_lo:[1,0,0] neg_hi:[1,0,0]
	v_exp_f32_e32 v96, v96
	v_exp_f32_e32 v97, v97
	v_exp_f32_e32 v98, v98
	v_exp_f32_e32 v99, v99
	v_exp_f32_e32 v100, v100
	v_exp_f32_e32 v101, v101
	v_exp_f32_e32 v102, v102
	v_exp_f32_e32 v103, v103
	v_pk_add_f32 v[82:83], v[82:83], v[104:105]
	v_pk_fma_f32 v[86:87], v[104:105], v[52:53], v[86:87]
	v_pk_add_f32 v[80:81], v[80:81], v[108:109]
	v_pk_add_f32 v[82:83], v[82:83], v[106:107]
	v_pk_fma_f32 v[86:87], v[106:107], v[54:55], v[86:87]
	v_pk_fma_f32 v[84:85], v[108:109], v[50:51], v[84:85] op_sel:[0,1,0] op_sel_hi:[1,0,1]
	v_pk_add_f32 v[82:83], v[82:83], v[110:111]
	v_pk_fma_f32 v[86:87], v[110:111], v[52:53], v[86:87] op_sel:[0,1,0] op_sel_hi:[1,0,1]
	v_pk_add_f32 v[104:105], v[52:53], v[44:45] neg_lo:[0,1] neg_hi:[0,1]
	v_pk_add_f32 v[106:107], v[54:55], v[44:45] neg_lo:[0,1] neg_hi:[0,1]
	v_pk_add_f32 v[108:109], v[50:51], v[42:43] op_sel:[1,0] op_sel_hi:[0,1] neg_lo:[0,1] neg_hi:[0,1]
	v_pk_add_f32 v[110:111], v[52:53], v[44:45] op_sel:[1,0] op_sel_hi:[0,1] neg_lo:[0,1] neg_hi:[0,1]
	v_pk_fma_f32 v[104:105], v[104:105], v[104:105], s[20:21] neg_lo:[1,0,0] neg_hi:[1,0,0]
	v_pk_fma_f32 v[106:107], v[106:107], v[106:107], s[26:27] neg_lo:[1,0,0] neg_hi:[1,0,0]
	v_pk_fma_f32 v[108:109], v[108:109], v[108:109], s[24:25] neg_lo:[1,0,0] neg_hi:[1,0,0]
	v_pk_fma_f32 v[110:111], v[110:111], v[110:111], s[24:25] neg_lo:[1,0,0] neg_hi:[1,0,0]
	v_exp_f32_e32 v104, v104
	v_exp_f32_e32 v105, v105
	v_exp_f32_e32 v106, v106
	v_exp_f32_e32 v107, v107
	v_exp_f32_e32 v108, v108
	v_exp_f32_e32 v109, v109
	v_exp_f32_e32 v110, v110
	v_exp_f32_e32 v111, v111
	v_pk_add_f32 v[88:89], v[88:89], v[96:97]
	v_pk_fma_f32 v[92:93], v[96:97], v[48:49], v[92:93]
	v_pk_add_f32 v[90:91], v[90:91], v[102:103]
	v_pk_add_f32 v[88:89], v[88:89], v[98:99]
	v_pk_fma_f32 v[92:93], v[98:99], v[50:51], v[92:93]
	v_pk_fma_f32 v[94:95], v[102:103], v[50:51], v[94:95]
	v_pk_add_f32 v[88:89], v[88:89], v[100:101]
	v_pk_fma_f32 v[92:93], v[100:101], v[52:53], v[92:93]
	v_sub_f32_e32 v96, v49, v34
	v_sub_f32_e32 v98, v52, v35
	v_sub_f32_e32 v100, v51, v36
	v_sub_f32_e32 v102, v54, v37
	v_sub_f32_e32 v97, v49, v42
	v_sub_f32_e32 v99, v52, v43
	v_sub_f32_e32 v101, v51, v44
	v_sub_f32_e32 v103, v54, v45
	v_fma_f32 v96, -v96, v96, s26
	v_fma_f32 v98, -v98, v98, s26
	v_fma_f32 v100, -v100, v100, s26
	v_fma_f32 v102, -v102, v102, s26
	v_fma_f32 v97, -v97, v97, s24
	v_fma_f32 v99, -v99, v99, s24
	v_fma_f32 v101, -v101, v101, s24
	v_fma_f32 v103, -v103, v103, s24
	v_exp_f32_e32 v96, v96
	v_exp_f32_e32 v98, v98
	v_exp_f32_e32 v100, v100
	v_exp_f32_e32 v102, v102
	v_exp_f32_e32 v97, v97
	v_exp_f32_e32 v99, v99
	v_exp_f32_e32 v101, v101
	v_exp_f32_e32 v103, v103
	v_pk_add_f32 v[90:91], v[90:91], v[104:105]
	v_pk_fma_f32 v[94:95], v[104:105], v[52:53], v[94:95]
	v_pk_add_f32 v[88:89], v[88:89], v[108:109]
	v_pk_add_f32 v[90:91], v[90:91], v[106:107]
	v_pk_fma_f32 v[94:95], v[106:107], v[54:55], v[94:95]
	v_pk_fma_f32 v[92:93], v[108:109], v[50:51], v[92:93] op_sel:[0,1,0] op_sel_hi:[1,0,1]
	v_pk_add_f32 v[90:91], v[90:91], v[110:111]
	v_pk_fma_f32 v[94:95], v[110:111], v[52:53], v[94:95] op_sel:[0,1,0] op_sel_hi:[1,0,1]
	v_add_f32_e32 v80, v80, v96
	v_fmac_f32_e32 v84, v96, v49
	v_add_f32_e32 v81, v81, v98
	v_fmac_f32_e32 v85, v98, v52
	v_add_f32_e32 v82, v82, v100
	v_fmac_f32_e32 v86, v100, v51
	v_add_f32_e32 v83, v83, v102
	v_fmac_f32_e32 v87, v102, v54
	v_add_f32_e32 v88, v88, v97
	v_fmac_f32_e32 v92, v97, v49
	v_add_f32_e32 v89, v89, v99
	v_fmac_f32_e32 v93, v99, v52
	v_add_f32_e32 v90, v90, v101
	v_fmac_f32_e32 v94, v101, v51
	v_add_f32_e32 v91, v91, v103
	v_fmac_f32_e32 v95, v103, v54
	v_rcp_f32_e32 v96, v80
	v_rcp_f32_e32 v97, v81
	v_rcp_f32_e32 v98, v82
	v_rcp_f32_e32 v99, v83
	v_pk_mul_f32 v[84:85], v[84:85], s[34:35]
	v_pk_mul_f32 v[86:87], v[86:87], s[34:35]
	v_pk_mul_f32 v[84:85], v[84:85], v[96:97]
	v_pk_mul_f32 v[86:87], v[86:87], v[98:99]
	buffer_store_dwordx4 v[84:87], v119, s[12:15], 0 offen sc1
	s_waitcnt vmcnt(3)
	s_nop 0
	v_mov_b32_dpp v56, v60 row_shr:1 row_mask:0xf bank_mask:0xf
	v_mov_b32_dpp v57, v61 row_shr:1 row_mask:0xf bank_mask:0xf
	v_mov_b32_dpp v62, v58 row_shl:1 row_mask:0xf bank_mask:0xf
	v_mov_b32_dpp v63, v59 row_shl:1 row_mask:0xf bank_mask:0xf
	v_pk_mul_f32 v[58:59], v[58:59], s[32:33]
	v_pk_mul_f32 v[60:61], v[60:61], s[32:33]
	v_cndmask_b32_e64 v57, v57, v56, vcc
	v_cndmask_b32_e64 v62, v62, v63, s[16:17]
	v_pk_mul_f32 v[56:57], v[56:57], s[32:33]
	v_pk_mul_f32 v[62:63], v[62:63], s[32:33]
	s_cmp_eq_u32 s19, 0
	s_cbranch_scc1 .Lmyha7
	s_setprio 0
	s_branch .Lmyhb7

.Lmyhb7:
	s_nop 0
	v_pk_add_f32 v[96:97], v[56:57], v[42:43] neg_lo:[0,1] neg_hi:[0,1]
	v_pk_add_f32 v[98:99], v[58:59], v[42:43] neg_lo:[0,1] neg_hi:[0,1]
	v_pk_add_f32 v[100:101], v[60:61], v[42:43] neg_lo:[0,1] neg_hi:[0,1]
	v_pk_add_f32 v[102:103], v[58:59], v[44:45] neg_lo:[0,1] neg_hi:[0,1]
	v_pk_fma_f32 v[96:97], v[96:97], v[96:97], s[28:29] neg_lo:[1,0,0] neg_hi:[1,0,0]
	v_pk_fma_f32 v[98:99], v[98:99], v[98:99], s[22:23] neg_lo:[1,0,0] neg_hi:[1,0,0]
	v_pk_fma_f32 v[100:101], v[100:101], v[100:101], s[28:29] neg_lo:[1,0,0] neg_hi:[1,0,0]
	v_pk_fma_f32 v[102:103], v[102:103], v[102:103], s[28:29] neg_lo:[1,0,0] neg_hi:[1,0,0]
	v_exp_f32_e32 v96, v96
	v_exp_f32_e32 v97, v97
	v_exp_f32_e32 v98, v98
	v_exp_f32_e32 v99, v99
	v_exp_f32_e32 v100, v100
	v_exp_f32_e32 v101, v101
	v_exp_f32_e32 v102, v102
	v_exp_f32_e32 v103, v103
	v_pk_add_f32 v[104:105], v[60:61], v[44:45] neg_lo:[0,1] neg_hi:[0,1]
	v_pk_add_f32 v[106:107], v[62:63], v[44:45] neg_lo:[0,1] neg_hi:[0,1]
	v_pk_add_f32 v[108:109], v[58:59], v[42:43] op_sel:[1,0] op_sel_hi:[0,1] neg_lo:[0,1] neg_hi:[0,1]
	v_pk_add_f32 v[110:111], v[60:61], v[44:45] op_sel:[1,0] op_sel_hi:[0,1] neg_lo:[0,1] neg_hi:[0,1]
	v_pk_fma_f32 v[104:105], v[104:105], v[104:105], s[22:23] neg_lo:[1,0,0] neg_hi:[1,0,0]
	v_pk_fma_f32 v[106:107], v[106:107], v[106:107], s[28:29] neg_lo:[1,0,0] neg_hi:[1,0,0]
	v_pk_fma_f32 v[108:109], v[108:109], v[108:109], s[26:27] neg_lo:[1,0,0] neg_hi:[1,0,0]
	v_pk_fma_f32 v[110:111], v[110:111], v[110:111], s[26:27] neg_lo:[1,0,0] neg_hi:[1,0,0]
	v_exp_f32_e32 v104, v104
	v_exp_f32_e32 v105, v105
	v_exp_f32_e32 v106, v106
	v_exp_f32_e32 v107, v107
	v_exp_f32_e32 v108, v108
	v_exp_f32_e32 v109, v109
	v_exp_f32_e32 v110, v110
	v_exp_f32_e32 v111, v111
	v_pk_add_f32 v[88:89], v[88:89], v[96:97]
	v_pk_fma_f32 v[92:93], v[96:97], v[56:57], v[92:93]
	v_pk_add_f32 v[90:91], v[90:91], v[102:103]
	v_pk_add_f32 v[88:89], v[88:89], v[98:99]
	v_pk_fma_f32 v[92:93], v[98:99], v[58:59], v[92:93]
	v_pk_fma_f32 v[94:95], v[102:103], v[58:59], v[94:95]
	v_pk_add_f32 v[88:89], v[88:89], v[100:101]
	v_pk_fma_f32 v[92:93], v[100:101], v[60:61], v[92:93]
	v_sub_f32_e32 v96, v57, v42
	v_sub_f32_e32 v98, v60, v43
	v_sub_f32_e32 v100, v59, v44
	v_sub_f32_e32 v102, v62, v45
	v_fma_f32 v96, -v96, v96, s26
	v_fma_f32 v98, -v98, v98, s26
	v_fma_f32 v100, -v100, v100, s26
	v_fma_f32 v102, -v102, v102, s26
	v_exp_f32_e32 v96, v96
	v_exp_f32_e32 v98, v98
	v_exp_f32_e32 v100, v100
	v_exp_f32_e32 v102, v102
	v_pk_add_f32 v[90:91], v[90:91], v[104:105]
	v_pk_fma_f32 v[94:95], v[104:105], v[60:61], v[94:95]
	v_pk_add_f32 v[88:89], v[88:89], v[108:109]
	v_pk_add_f32 v[90:91], v[90:91], v[106:107]
	v_pk_fma_f32 v[94:95], v[106:107], v[62:63], v[94:95]
	v_pk_fma_f32 v[92:93], v[108:109], v[58:59], v[92:93] op_sel:[0,1,0] op_sel_hi:[1,0,1]
	v_pk_add_f32 v[90:91], v[90:91], v[110:111]
	v_pk_fma_f32 v[94:95], v[110:111], v[60:61], v[94:95] op_sel:[0,1,0] op_sel_hi:[1,0,1]
	v_add_f32_e32 v88, v88, v96
	v_fmac_f32_e32 v92, v96, v57
	v_add_f32_e32 v89, v89, v98
	v_fmac_f32_e32 v93, v98, v60
	v_add_f32_e32 v90, v90, v100
	v_fmac_f32_e32 v94, v100, v59
	v_add_f32_e32 v91, v91, v102
	v_fmac_f32_e32 v95, v102, v62
	v_rcp_f32_e32 v96, v88
	v_rcp_f32_e32 v97, v89
	v_rcp_f32_e32 v98, v90
	v_rcp_f32_e32 v99, v91
	v_pk_mul_f32 v[92:93], v[92:93], s[34:35]
	v_pk_mul_f32 v[94:95], v[94:95], s[34:35]
	v_pk_mul_f32 v[92:93], v[92:93], v[96:97]
	v_pk_mul_f32 v[94:95], v[94:95], v[98:99]
	buffer_store_dwordx4 v[92:95], v119, s[12:15], 0 offen offset:2048 sc1
	s_endpgm
